# nt hint extended to the read-once activation loads: w_o0 epilogue residual, router x1, combine YB/x1 rows
# speedup vs baseline: 1.0038x; 1.0038x over previous
.LBB0_705:
	s_cmp_gt_i32 s44, 63
	v_lshl_or_b32 v130, s67, 8, v169
	s_cselect_b32 s39, s66, 0x700000
	s_cselect_b32 s47, s23, s21
	s_cselect_b32 s46, s22, s20
	s_cselect_b32 s37, 0xffffc000, 0
	s_add_u32 s48, s18, s39
	v_ashrrev_i32_e32 v131, 31, v130
	s_addc_u32 s49, s19, 0
	v_lshlrev_b64 v[132:133], 2, v[130:131]
	v_lshl_add_u32 v166, s44, 8, v1
	v_lshl_add_u64 v[134:135], s[48:49], 0, v[132:133]
	v_lshl_add_u64 v[162:163], s[46:47], 0, v[132:133]
	v_add_u32_e32 v132, s37, v166
	v_ashrrev_i32_e32 v133, 31, v132
	v_lshlrev_b64 v[132:133], 13, v[132:133]
	v_lshl_add_u64 v[182:183], v[134:135], 0, s[34:35]
	v_add_co_u32_e32 v134, vcc, s57, v134
	v_lshl_add_u64 v[184:185], v[162:163], 0, v[132:133]
	s_nop 0
	v_addc_co_u32_e32 v135, vcc, 0, v135, vcc
	global_load_dwordx4 v[138:141], v[182:183], off offset:16 nt
	global_load_dwordx4 v[174:177], v[184:185], off offset:16 nt
	global_load_dwordx4 v[178:181], v[184:185], off nt
	global_load_dwordx4 v[142:145], v[134:135], off nt
	v_ashrrev_i32_e32 v167, 31, v166
	v_lshlrev_b64 v[132:133], 12, v[166:167]
	v_lshlrev_b64 v[164:165], 1, v[130:131]
	v_lshl_add_u64 v[130:131], s[26:27], 0, v[132:133]
	v_lshl_add_u64 v[186:187], v[130:131], 0, v[164:165]
	global_load_dwordx4 v[134:137], v[182:183], off offset:512 nt
	global_load_dwordx4 v[130:133], v[182:183], off offset:528 nt
	s_andn2_b64 vcc, exec, s[6:7]
	s_mov_b64 s[6:7], -1
	s_waitcnt vmcnt(0)
	v_pk_fma_f32 v[176:177], v[124:125], v[140:141], v[176:177]
	v_pk_fma_f32 v[124:125], v[122:123], v[138:139], v[174:175]
	v_pk_fma_f32 v[122:123], v[126:127], v[142:143], v[178:179]
	v_pk_fma_f32 v[128:129], v[128:129], v[144:145], v[180:181]
	v_cvt_pk_bf16_f32 v122, v122, v123
	v_or_b32_e32 v174, 16, v166
	v_cvt_pk_bf16_f32 v123, v128, v129
	v_cvt_pk_bf16_f32 v124, v124, v125
	v_cvt_pk_bf16_f32 v125, v176, v177
	global_store_dwordx4 v[186:187], v[122:125], off
	global_load_dwordx4 v[122:125], v[184:185], off offset:512 nt
	s_nop 0
	global_load_dwordx4 v[126:129], v[184:185], off offset:528 nt
	v_add_u32_e32 v176, s37, v174
	v_ashrrev_i32_e32 v177, 31, v176
	v_lshlrev_b64 v[176:177], 13, v[176:177]
	v_lshl_add_u64 v[176:177], v[162:163], 0, v[176:177]
	v_ashrrev_i32_e32 v175, 31, v174
	s_waitcnt vmcnt(1)
	v_pk_fma_f32 v[114:115], v[114:115], v[134:135], v[122:123]
	s_waitcnt vmcnt(0)
	v_pk_fma_f32 v[122:123], v[108:109], v[132:133], v[128:129]
	v_pk_fma_f32 v[108:109], v[106:107], v[130:131], v[126:127]
	v_pk_fma_f32 v[116:117], v[116:117], v[136:137], v[124:125]
	v_cvt_pk_bf16_f32 v106, v114, v115
	s_nop 0
	v_cvt_pk_bf16_f32 v107, v116, v117
	v_cvt_pk_bf16_f32 v108, v108, v109
	v_cvt_pk_bf16_f32 v109, v122, v123
	global_store_dwordx4 v[186:187], v[106:109], off offset:256
	global_load_dwordx4 v[106:109], v[176:177], off nt
	s_nop 0
	global_load_dwordx4 v[114:117], v[176:177], off offset:16 nt
	v_lshlrev_b64 v[122:123], 12, v[174:175]
	v_lshl_add_u64 v[122:123], s[26:27], 0, v[122:123]
	v_lshl_add_u64 v[122:123], v[122:123], 0, v[164:165]
	s_waitcnt vmcnt(1)
	v_pk_fma_f32 v[108:109], v[120:121], v[144:145], v[108:109]
	v_pk_fma_f32 v[106:107], v[118:119], v[142:143], v[106:107]
	s_waitcnt vmcnt(0)
	v_pk_fma_f32 v[112:113], v[112:113], v[140:141], v[116:117]
	v_pk_fma_f32 v[110:111], v[110:111], v[138:139], v[114:115]
	v_cvt_pk_bf16_f32 v106, v106, v107
	v_cvt_pk_bf16_f32 v107, v108, v109
	v_or_b32_e32 v114, 32, v166
	v_cvt_pk_bf16_f32 v108, v110, v111
	v_cvt_pk_bf16_f32 v109, v112, v113
	global_store_dwordx4 v[122:123], v[106:109], off
	global_load_dwordx4 v[106:109], v[176:177], off offset:512 nt
	s_nop 0
	global_load_dwordx4 v[110:113], v[176:177], off offset:528 nt
	v_add_u32_e32 v116, s37, v114
	v_ashrrev_i32_e32 v117, 31, v116
	v_lshlrev_b64 v[116:117], 13, v[116:117]
	v_lshl_add_u64 v[116:117], v[162:163], 0, v[116:117]
	v_ashrrev_i32_e32 v115, 31, v114
	s_waitcnt vmcnt(1)
	v_pk_fma_f32 v[98:99], v[98:99], v[134:135], v[106:107]
	s_waitcnt vmcnt(0)
	v_pk_fma_f32 v[106:107], v[92:93], v[132:133], v[112:113]
	v_pk_fma_f32 v[92:93], v[90:91], v[130:131], v[110:111]
	v_pk_fma_f32 v[100:101], v[100:101], v[136:137], v[108:109]
	v_cvt_pk_bf16_f32 v90, v98, v99
	s_nop 0
	v_cvt_pk_bf16_f32 v91, v100, v101
	v_cvt_pk_bf16_f32 v92, v92, v93
	v_cvt_pk_bf16_f32 v93, v106, v107
	global_store_dwordx4 v[122:123], v[90:93], off offset:256
	global_load_dwordx4 v[90:93], v[116:117], off nt
	s_nop 0
	global_load_dwordx4 v[98:101], v[116:117], off offset:16 nt
	v_lshlrev_b64 v[106:107], 12, v[114:115]
	v_lshl_add_u64 v[106:107], s[26:27], 0, v[106:107]
	v_lshl_add_u64 v[106:107], v[106:107], 0, v[164:165]
	s_waitcnt vmcnt(1)
	v_pk_fma_f32 v[92:93], v[104:105], v[144:145], v[92:93]
	v_pk_fma_f32 v[90:91], v[102:103], v[142:143], v[90:91]
	s_waitcnt vmcnt(0)
	v_pk_fma_f32 v[96:97], v[96:97], v[140:141], v[100:101]
	v_pk_fma_f32 v[94:95], v[94:95], v[138:139], v[98:99]
	v_cvt_pk_bf16_f32 v90, v90, v91
	v_cvt_pk_bf16_f32 v91, v92, v93
	v_or_b32_e32 v98, 48, v166
	v_cvt_pk_bf16_f32 v92, v94, v95
	v_cvt_pk_bf16_f32 v93, v96, v97
	global_store_dwordx4 v[106:107], v[90:93], off
	global_load_dwordx4 v[90:93], v[116:117], off offset:512 nt
	s_nop 0
	global_load_dwordx4 v[94:97], v[116:117], off offset:528 nt
	v_add_u32_e32 v100, s37, v98
	v_ashrrev_i32_e32 v101, 31, v100
	v_lshlrev_b64 v[100:101], 13, v[100:101]
	v_lshl_add_u64 v[100:101], v[162:163], 0, v[100:101]
	v_ashrrev_i32_e32 v99, 31, v98
	s_waitcnt vmcnt(1)
	v_pk_fma_f32 v[82:83], v[82:83], v[134:135], v[90:91]
	s_waitcnt vmcnt(0)
	v_pk_fma_f32 v[90:91], v[76:77], v[132:133], v[96:97]
	v_pk_fma_f32 v[76:77], v[74:75], v[130:131], v[94:95]
	v_pk_fma_f32 v[84:85], v[84:85], v[136:137], v[92:93]
	v_cvt_pk_bf16_f32 v74, v82, v83
	s_nop 0
	v_cvt_pk_bf16_f32 v75, v84, v85
	v_cvt_pk_bf16_f32 v76, v76, v77
	v_cvt_pk_bf16_f32 v77, v90, v91
	global_store_dwordx4 v[106:107], v[74:77], off offset:256
	global_load_dwordx4 v[74:77], v[100:101], off nt
	s_nop 0
	global_load_dwordx4 v[82:85], v[100:101], off offset:16 nt
	v_lshlrev_b64 v[90:91], 12, v[98:99]
	v_lshl_add_u64 v[90:91], s[26:27], 0, v[90:91]
	v_lshl_add_u64 v[90:91], v[90:91], 0, v[164:165]
	s_waitcnt vmcnt(1)
	v_pk_fma_f32 v[76:77], v[88:89], v[144:145], v[76:77]
	v_pk_fma_f32 v[74:75], v[86:87], v[142:143], v[74:75]
	s_waitcnt vmcnt(0)
	v_pk_fma_f32 v[80:81], v[80:81], v[140:141], v[84:85]
	v_pk_fma_f32 v[78:79], v[78:79], v[138:139], v[82:83]
	v_cvt_pk_bf16_f32 v74, v74, v75
	v_cvt_pk_bf16_f32 v75, v76, v77
	v_add_u32_e32 v82, 0x80, v166
	v_cvt_pk_bf16_f32 v76, v78, v79
	v_cvt_pk_bf16_f32 v77, v80, v81
	global_store_dwordx4 v[90:91], v[74:77], off
	global_load_dwordx4 v[74:77], v[100:101], off offset:512 nt
	s_nop 0
	global_load_dwordx4 v[78:81], v[100:101], off offset:528 nt
	v_add_u32_e32 v84, s37, v82
	v_ashrrev_i32_e32 v85, 31, v84
	v_lshlrev_b64 v[84:85], 13, v[84:85]
	v_lshl_add_u64 v[84:85], v[162:163], 0, v[84:85]
	v_ashrrev_i32_e32 v83, 31, v82
	s_waitcnt vmcnt(1)
	v_pk_fma_f32 v[70:71], v[70:71], v[134:135], v[74:75]
	s_waitcnt vmcnt(0)
	v_pk_fma_f32 v[74:75], v[68:69], v[132:133], v[80:81]
	v_pk_fma_f32 v[68:69], v[66:67], v[130:131], v[78:79]
	v_pk_fma_f32 v[72:73], v[72:73], v[136:137], v[76:77]
	v_cvt_pk_bf16_f32 v66, v70, v71
	s_nop 0
	v_cvt_pk_bf16_f32 v67, v72, v73
	v_cvt_pk_bf16_f32 v68, v68, v69
	v_cvt_pk_bf16_f32 v69, v74, v75
	global_store_dwordx4 v[90:91], v[66:69], off offset:256
	global_load_dwordx4 v[66:69], v[84:85], off nt
	s_nop 0
	global_load_dwordx4 v[70:73], v[84:85], off offset:16 nt
	v_lshlrev_b64 v[74:75], 12, v[82:83]
	v_lshl_add_u64 v[74:75], s[26:27], 0, v[74:75]
	v_lshl_add_u64 v[74:75], v[74:75], 0, v[164:165]
	s_waitcnt vmcnt(1)
	v_pk_fma_f32 v[62:63], v[62:63], v[142:143], v[66:67]
	s_waitcnt vmcnt(0)
	v_pk_fma_f32 v[66:67], v[60:61], v[140:141], v[72:73]
	v_pk_fma_f32 v[60:61], v[58:59], v[138:139], v[70:71]
	v_pk_fma_f32 v[64:65], v[64:65], v[144:145], v[68:69]
	v_cvt_pk_bf16_f32 v58, v62, v63
	s_nop 0
	v_cvt_pk_bf16_f32 v59, v64, v65
	v_cvt_pk_bf16_f32 v60, v60, v61
	v_cvt_pk_bf16_f32 v61, v66, v67
	global_store_dwordx4 v[74:75], v[58:61], off
	global_load_dwordx4 v[58:61], v[84:85], off offset:512 nt
	s_nop 0
	global_load_dwordx4 v[62:65], v[84:85], off offset:528 nt
	v_add_u32_e32 v66, 0x90, v166
	v_add_u32_e32 v68, s37, v66
	v_ashrrev_i32_e32 v69, 31, v68
	v_lshlrev_b64 v[68:69], 13, v[68:69]
	v_lshl_add_u64 v[68:69], v[162:163], 0, v[68:69]
	v_ashrrev_i32_e32 v67, 31, v66
	s_waitcnt vmcnt(1)
	v_pk_fma_f32 v[50:51], v[50:51], v[134:135], v[58:59]
	s_waitcnt vmcnt(0)
	v_pk_fma_f32 v[58:59], v[44:45], v[132:133], v[64:65]
	v_pk_fma_f32 v[44:45], v[42:43], v[130:131], v[62:63]
	v_pk_fma_f32 v[52:53], v[52:53], v[136:137], v[60:61]
	v_cvt_pk_bf16_f32 v42, v50, v51
	s_nop 0
	v_cvt_pk_bf16_f32 v43, v52, v53
	v_cvt_pk_bf16_f32 v44, v44, v45
	v_cvt_pk_bf16_f32 v45, v58, v59
	global_store_dwordx4 v[74:75], v[42:45], off offset:256
	global_load_dwordx4 v[42:45], v[68:69], off nt
	s_nop 0
	global_load_dwordx4 v[50:53], v[68:69], off offset:16 nt
	v_lshlrev_b64 v[58:59], 12, v[66:67]
	v_lshl_add_u64 v[58:59], s[26:27], 0, v[58:59]
	v_lshl_add_u64 v[58:59], v[58:59], 0, v[164:165]
	s_waitcnt vmcnt(1)
	v_pk_fma_f32 v[44:45], v[56:57], v[144:145], v[44:45]
	v_pk_fma_f32 v[42:43], v[54:55], v[142:143], v[42:43]
	s_waitcnt vmcnt(0)
	v_pk_fma_f32 v[48:49], v[48:49], v[140:141], v[52:53]
	v_pk_fma_f32 v[46:47], v[46:47], v[138:139], v[50:51]
	v_cvt_pk_bf16_f32 v42, v42, v43
	v_cvt_pk_bf16_f32 v43, v44, v45
	v_add_u32_e32 v50, 0xa0, v166
	v_cvt_pk_bf16_f32 v44, v46, v47
	v_cvt_pk_bf16_f32 v45, v48, v49
	global_store_dwordx4 v[58:59], v[42:45], off
	global_load_dwordx4 v[42:45], v[68:69], off offset:512 nt
	s_nop 0
	global_load_dwordx4 v[46:49], v[68:69], off offset:528 nt
	v_add_u32_e32 v52, s37, v50
	v_ashrrev_i32_e32 v53, 31, v52
	v_lshlrev_b64 v[52:53], 13, v[52:53]
	v_lshl_add_u64 v[52:53], v[162:163], 0, v[52:53]
	v_ashrrev_i32_e32 v51, 31, v50
	s_waitcnt vmcnt(1)
	v_pk_fma_f32 v[34:35], v[34:35], v[134:135], v[42:43]
	s_waitcnt vmcnt(0)
	v_pk_fma_f32 v[42:43], v[28:29], v[132:133], v[48:49]
	v_pk_fma_f32 v[28:29], v[26:27], v[130:131], v[46:47]
	v_pk_fma_f32 v[36:37], v[36:37], v[136:137], v[44:45]
	v_cvt_pk_bf16_f32 v26, v34, v35
	s_nop 0
	v_cvt_pk_bf16_f32 v27, v36, v37
	v_cvt_pk_bf16_f32 v28, v28, v29
	v_cvt_pk_bf16_f32 v29, v42, v43
	global_store_dwordx4 v[58:59], v[26:29], off offset:256
	global_load_dwordx4 v[26:29], v[52:53], off nt
	s_nop 0
	global_load_dwordx4 v[34:37], v[52:53], off offset:16 nt
	v_lshlrev_b64 v[42:43], 12, v[50:51]
	v_lshl_add_u64 v[42:43], s[26:27], 0, v[42:43]
	v_lshl_add_u64 v[42:43], v[42:43], 0, v[164:165]
	s_waitcnt vmcnt(1)
	v_pk_fma_f32 v[28:29], v[40:41], v[144:145], v[28:29]
	v_pk_fma_f32 v[26:27], v[38:39], v[142:143], v[26:27]
	s_waitcnt vmcnt(0)
	v_pk_fma_f32 v[32:33], v[32:33], v[140:141], v[36:37]
	v_pk_fma_f32 v[30:31], v[30:31], v[138:139], v[34:35]
	v_cvt_pk_bf16_f32 v26, v26, v27
	v_cvt_pk_bf16_f32 v27, v28, v29
	v_add_u32_e32 v34, 0xb0, v166
	v_cvt_pk_bf16_f32 v28, v30, v31
	v_cvt_pk_bf16_f32 v29, v32, v33
	global_store_dwordx4 v[42:43], v[26:29], off
	global_load_dwordx4 v[26:29], v[52:53], off offset:512 nt
	s_nop 0
	global_load_dwordx4 v[30:33], v[52:53], off offset:528 nt
	v_add_u32_e32 v36, s37, v34
	v_ashrrev_i32_e32 v37, 31, v36
	v_lshlrev_b64 v[36:37], 13, v[36:37]
	v_lshl_add_u64 v[36:37], v[162:163], 0, v[36:37]
	v_ashrrev_i32_e32 v35, 31, v34
	s_waitcnt vmcnt(1)
	v_pk_fma_f32 v[18:19], v[18:19], v[134:135], v[26:27]
	s_waitcnt vmcnt(0)
	v_pk_fma_f32 v[26:27], v[12:13], v[132:133], v[32:33]
	v_pk_fma_f32 v[12:13], v[10:11], v[130:131], v[30:31]
	v_pk_fma_f32 v[20:21], v[20:21], v[136:137], v[28:29]
	v_cvt_pk_bf16_f32 v10, v18, v19
	s_nop 0
	v_cvt_pk_bf16_f32 v11, v20, v21
	v_cvt_pk_bf16_f32 v12, v12, v13
	v_cvt_pk_bf16_f32 v13, v26, v27
	global_store_dwordx4 v[42:43], v[10:13], off offset:256
	global_load_dwordx4 v[10:13], v[36:37], off nt
	s_nop 0
	global_load_dwordx4 v[18:21], v[36:37], off offset:16 nt
	v_lshlrev_b64 v[26:27], 12, v[34:35]
	v_lshl_add_u64 v[26:27], s[26:27], 0, v[26:27]
	v_lshl_add_u64 v[26:27], v[26:27], 0, v[164:165]
	s_waitcnt vmcnt(1)
	v_pk_fma_f32 v[12:13], v[24:25], v[144:145], v[12:13]
	v_pk_fma_f32 v[10:11], v[22:23], v[142:143], v[10:11]
	s_waitcnt vmcnt(0)
	v_pk_fma_f32 v[16:17], v[16:17], v[140:141], v[20:21]
	v_pk_fma_f32 v[14:15], v[14:15], v[138:139], v[18:19]
	v_cvt_pk_bf16_f32 v10, v10, v11
	v_cvt_pk_bf16_f32 v11, v12, v13
	s_nop 0
	v_cvt_pk_bf16_f32 v12, v14, v15
	v_cvt_pk_bf16_f32 v13, v16, v17
	global_store_dwordx4 v[26:27], v[10:13], off
	global_load_dwordx4 v[10:13], v[36:37], off offset:512 nt
	s_nop 0
	global_load_dwordx4 v[14:17], v[36:37], off offset:528 nt
	s_waitcnt vmcnt(1)
	v_pk_fma_f32 v[6:7], v[6:7], v[134:135], v[10:11]
	s_waitcnt vmcnt(0)
	v_pk_fma_f32 v[10:11], v[4:5], v[132:133], v[16:17]
	v_pk_fma_f32 v[4:5], v[2:3], v[130:131], v[14:15]
	v_pk_fma_f32 v[8:9], v[8:9], v[136:137], v[12:13]
	v_cvt_pk_bf16_f32 v2, v6, v7
	s_nop 0
	v_cvt_pk_bf16_f32 v3, v8, v9
	v_cvt_pk_bf16_f32 v4, v4, v5
	v_cvt_pk_bf16_f32 v5, v10, v11
	global_store_dwordx4 v[26:27], v[2:5], off offset:256
	s_cbranch_vccnz .LBB0_698
	s_andn2_b64 vcc, exec, s[24:25]
	s_cbranch_vccnz .LBB0_697
	s_barrier
	s_branch .LBB0_697

.LBB0_797:
	v_readlane_b32 s0, v253, 11
	v_readlane_b32 s1, v253, 12
	s_mov_b32 s3, s1
	s_cmp_lt_i32 s0, 10
	s_cselect_b64 s[0:1], -1, 0
	s_cmp_gt_i32 s3, 9
	s_cselect_b64 s[4:5], -1, 0
	s_and_b64 s[0:1], s[0:1], s[4:5]
	s_andn2_b64 vcc, exec, s[0:1]
	s_cbranch_vccnz .LBB0_811
	v_readlane_b32 s0, v253, 0
	v_readlane_b32 s1, v253, 1
	s_load_dwordx2 s[12:13], s[0:1], 0x38
	s_load_dwordx2 s[4:5], s[0:1], 0xa8
	s_load_dwordx2 s[8:9], s[0:1], 0xd0
	v_mov_b32_e32 v1, v0
	s_mov_b32 s1, 0x708000
	v_lshlrev_b32_e32 v2, 2, v1
	v_ashrrev_i32_e32 v3, 31, v2
	v_lshlrev_b64 v[6:7], 2, v[2:3]
	s_waitcnt lgkmcnt(0)
	v_lshl_add_u64 v[2:3], s[12:13], 0, v[6:7]
	v_lshl_add_u64 v[6:7], s[8:9], 0, v[6:7]
	v_add_co_u32_e32 v14, vcc, s1, v6
	s_mov_b32 s1, 0x706000
	s_nop 0
	v_addc_co_u32_e32 v15, vcc, 0, v7, vcc
	v_add_co_u32_e32 v16, vcc, s1, v6
	global_load_dwordx4 v[2:5], v[2:3], off nt
	s_nop 0
	v_addc_co_u32_e32 v17, vcc, 0, v7, vcc
	global_load_dwordx4 v[6:9], v[14:15], off nt
	global_load_dwordx4 v[10:13], v[16:17], off nt
	v_readfirstlane_b32 s0, v1
	v_lshrrev_b32_e32 v14, 1, v1
	s_ashr_i32 s0, s0, 6
	v_and_b32_e32 v14, 24, v14
	v_lshl_or_b32 v14, s0, 8, v14
	v_ashrrev_i32_e32 v15, 31, v14
	v_lshlrev_b64 v[14:15], 6, v[14:15]
	v_and_b32_e32 v16, 15, v1
	v_lshl_add_u64 v[14:15], s[4:5], 0, v[14:15]
	v_lshlrev_b32_e32 v66, 2, v16
	v_mov_b32_e32 v67, 0
	v_lshl_add_u64 v[18:19], v[14:15], 0, v[66:67]
	global_load_dword v16, v[18:19], off
	global_load_dword v17, v[18:19], off offset:64
	global_load_dword v20, v[18:19], off offset:128
	global_load_dword v21, v[18:19], off offset:192
	global_load_dword v24, v[18:19], off offset:256
	global_load_dword v25, v[18:19], off offset:320
	global_load_dword v26, v[18:19], off offset:384
	global_load_dword v27, v[18:19], off offset:448
	global_load_dword v28, v[18:19], off offset:2048
	global_load_dword v29, v[18:19], off offset:2112
	global_load_dword v30, v[18:19], off offset:2176
	global_load_dword v31, v[18:19], off offset:2240
	global_load_dword v32, v[18:19], off offset:2304
	global_load_dword v33, v[18:19], off offset:2368
	global_load_dword v34, v[18:19], off offset:2432
	global_load_dword v35, v[18:19], off offset:2496
	s_movk_i32 s3, 0x1000
	v_lshl_add_u32 v14, v1, 4, 0
	v_add_u32_e32 v36, 0x20000, v14
	v_add_u32_e32 v37, 0x22000, v14
	v_add_co_u32_e32 v14, vcc, s3, v18
	s_movk_i32 s4, 0x2000
	s_nop 0
	v_addc_co_u32_e32 v15, vcc, 0, v19, vcc
	v_add_co_u32_e32 v22, vcc, s4, v18
	s_movk_i32 s3, 0x3000
	s_nop 0
	v_addc_co_u32_e32 v23, vcc, 0, v19, vcc
	global_load_dword v38, v[22:23], off offset:-4096
	global_load_dword v39, v[14:15], off offset:64
	global_load_dword v40, v[14:15], off offset:128
	global_load_dword v41, v[14:15], off offset:192
	global_load_dword v42, v[14:15], off offset:256
	global_load_dword v43, v[14:15], off offset:320
	global_load_dword v44, v[14:15], off offset:384
	global_load_dword v45, v[14:15], off offset:448
	s_lshl_b32 s10, s60, 3
	s_lshl_b32 s1, s2, 3
	v_and_b32_e32 v1, 63, v1
	s_cmpk_gt_i32 s2, 0x7ff
	s_waitcnt vmcnt(25)
	v_pk_add_f32 v[8:9], v[8:9], 1.0 op_sel_hi:[1,0]
	v_pk_add_f32 v[6:7], v[6:7], 1.0 op_sel_hi:[1,0]
	v_pk_mul_f32 v[8:9], v[4:5], v[8:9]
	v_pk_mul_f32 v[6:7], v[2:3], v[6:7]
	s_waitcnt vmcnt(24)
	ds_write_b128 v37, v[10:13]
	ds_write_b128 v36, v[6:9]
	global_load_dword v36, v[14:15], off offset:2048
	global_load_dword v37, v[14:15], off offset:2112
	global_load_dword v46, v[14:15], off offset:2176
	global_load_dword v47, v[14:15], off offset:2240
	global_load_dword v48, v[14:15], off offset:2304
	global_load_dword v49, v[14:15], off offset:2368
	global_load_dword v50, v[14:15], off offset:2432
	global_load_dword v51, v[14:15], off offset:2496
	s_waitcnt vmcnt(30)
	v_cvt_pk_bf16_f32 v2, v16, v17
	s_waitcnt vmcnt(28)
	v_cvt_pk_bf16_f32 v3, v20, v21
	s_waitcnt vmcnt(26)
	v_cvt_pk_bf16_f32 v4, v24, v25
	s_waitcnt vmcnt(24)
	v_cvt_pk_bf16_f32 v5, v26, v27
	global_load_dword v52, v[22:23], off
	global_load_dword v53, v[22:23], off offset:64
	global_load_dword v54, v[22:23], off offset:128
	global_load_dword v55, v[22:23], off offset:192
	global_load_dword v56, v[22:23], off offset:256
	global_load_dword v57, v[22:23], off offset:320
	global_load_dword v58, v[22:23], off offset:384
	global_load_dword v59, v[22:23], off offset:448
	v_lshlrev_b32_e32 v6, 16, v2
	v_and_b32_e32 v7, 0xffff0000, v2
	v_sub_f32_e32 v6, v16, v6
	v_sub_f32_e32 v7, v17, v7
	v_lshlrev_b32_e32 v8, 16, v3
	v_cvt_pk_bf16_f32 v6, v6, v7
	v_and_b32_e32 v7, 0xffff0000, v3
	v_sub_f32_e32 v8, v20, v8
	v_sub_f32_e32 v7, v21, v7
	v_cvt_pk_bf16_f32 v7, v8, v7
	v_lshlrev_b32_e32 v8, 16, v4
	v_and_b32_e32 v9, 0xffff0000, v4
	v_sub_f32_e32 v8, v24, v8
	v_sub_f32_e32 v9, v25, v9
	v_cvt_pk_bf16_f32 v8, v8, v9
	v_lshlrev_b32_e32 v9, 16, v5
	v_and_b32_e32 v10, 0xffff0000, v5
	v_sub_f32_e32 v9, v26, v9
	v_sub_f32_e32 v10, v27, v10
	v_cvt_pk_bf16_f32 v9, v9, v10
	s_waitcnt vmcnt(30)
	v_cvt_pk_bf16_f32 v10, v28, v29
	s_waitcnt vmcnt(28)
	v_cvt_pk_bf16_f32 v11, v30, v31
	s_waitcnt vmcnt(26)
	v_cvt_pk_bf16_f32 v12, v32, v33
	s_waitcnt vmcnt(24)
	v_cvt_pk_bf16_f32 v13, v34, v35
	s_waitcnt vmcnt(16)
	v_cvt_pk_bf16_f32 v21, v44, v45
	s_waitcnt vmcnt(12)
	v_cvt_pk_bf16_f32 v27, v46, v47
	v_lshlrev_b32_e32 v16, 16, v10
	v_sub_f32_e32 v16, v28, v16
	v_and_b32_e32 v17, 0xffff0000, v10
	v_sub_f32_e32 v17, v29, v17
	v_cvt_pk_bf16_f32 v14, v16, v17
	v_lshlrev_b32_e32 v15, 16, v11
	v_and_b32_e32 v16, 0xffff0000, v11
	v_sub_f32_e32 v15, v30, v15
	v_sub_f32_e32 v16, v31, v16
	v_cvt_pk_bf16_f32 v15, v15, v16
	v_lshlrev_b32_e32 v16, 16, v12
	v_sub_f32_e32 v16, v32, v16
	v_and_b32_e32 v17, 0xffff0000, v12
	v_add_co_u32_e32 v32, vcc, s3, v18
	v_sub_f32_e32 v17, v33, v17
	s_nop 0
	v_addc_co_u32_e32 v33, vcc, 0, v19, vcc
	global_load_dword v62, v[32:33], off offset:2112
	global_load_dword v63, v[32:33], off offset:2176
	global_load_dword v64, v[32:33], off offset:2240
	global_load_dword v65, v[32:33], off offset:2304
	global_load_dword v66, v[32:33], off offset:2368
	global_load_dword v68, v[32:33], off offset:2432
	global_load_dword v69, v[32:33], off offset:2496
	global_load_dword v60, v[22:23], off offset:2048
	global_load_dword v61, v[22:23], off offset:2112
	global_load_dword v70, v[22:23], off offset:2176
	global_load_dword v71, v[22:23], off offset:2240
	global_load_dword v72, v[22:23], off offset:2304
	global_load_dword v73, v[22:23], off offset:2368
	global_load_dword v74, v[22:23], off offset:2432
	global_load_dword v75, v[22:23], off offset:2496
	global_load_dword v76, v[32:33], off
	global_load_dword v77, v[32:33], off offset:64
	global_load_dword v78, v[32:33], off offset:128
	global_load_dword v79, v[32:33], off offset:192
	global_load_dword v80, v[32:33], off offset:256
	global_load_dword v81, v[32:33], off offset:320
	global_load_dword v82, v[32:33], off offset:384
	global_load_dword v83, v[32:33], off offset:448
	global_load_dword v84, v[32:33], off offset:2048
	v_cvt_pk_bf16_f32 v18, v38, v39
	v_cvt_pk_bf16_f32 v16, v16, v17
	v_lshlrev_b32_e32 v17, 16, v13
	v_lshlrev_b32_e32 v24, 16, v18
	v_and_b32_e32 v23, 0xffff0000, v18
	v_sub_f32_e32 v22, v38, v24
	v_sub_f32_e32 v23, v39, v23
	v_and_b32_e32 v20, 0xffff0000, v13
	v_cvt_pk_bf16_f32 v19, v40, v41
	v_cvt_pk_bf16_f32 v22, v22, v23
	v_sub_f32_e32 v17, v34, v17
	v_lshlrev_b32_e32 v23, 16, v19
	v_and_b32_e32 v24, 0xffff0000, v19
	v_sub_f32_e32 v20, v35, v20
	v_sub_f32_e32 v23, v40, v23
	v_sub_f32_e32 v24, v41, v24
	v_cvt_pk_bf16_f32 v17, v17, v20
	v_cvt_pk_bf16_f32 v20, v42, v43
	v_cvt_pk_bf16_f32 v23, v23, v24
	v_and_b32_e32 v26, 0xffff0000, v21
	v_lshlrev_b32_e32 v24, 16, v20
	v_and_b32_e32 v25, 0xffff0000, v20
	v_sub_f32_e32 v24, v42, v24
	v_sub_f32_e32 v25, v43, v25
	v_cvt_pk_bf16_f32 v24, v24, v25
	v_lshlrev_b32_e32 v25, 16, v21
	v_sub_f32_e32 v25, v44, v25
	v_sub_f32_e32 v26, v45, v26
	v_cvt_pk_bf16_f32 v25, v25, v26
	v_cvt_pk_bf16_f32 v26, v36, v37
	v_and_b32_e32 v34, 0xffff0000, v27
	v_lshlrev_b32_e32 v30, 16, v26
	v_and_b32_e32 v31, 0xffff0000, v26
	v_sub_f32_e32 v30, v36, v30
	v_sub_f32_e32 v31, v37, v31
	v_cvt_pk_bf16_f32 v30, v30, v31
	v_lshlrev_b32_e32 v31, 16, v27
	v_sub_f32_e32 v31, v46, v31
	v_sub_f32_e32 v34, v47, v34
	s_waitcnt vmcnt(34)
	v_cvt_pk_bf16_f32 v28, v48, v49
	v_cvt_pk_bf16_f32 v31, v31, v34
	s_waitcnt vmcnt(32)
	v_cvt_pk_bf16_f32 v29, v50, v51
	s_waitcnt vmcnt(26)
	v_cvt_pk_bf16_f32 v36, v56, v57
	s_waitcnt vmcnt(24)
	v_cvt_pk_bf16_f32 v37, v58, v59
	s_waitcnt vmcnt(13)
	v_cvt_pk_bf16_f32 v43, v70, v71
	v_lshlrev_b32_e32 v34, 16, v28
	v_and_b32_e32 v35, 0xffff0000, v28
	v_sub_f32_e32 v34, v48, v34
	v_sub_f32_e32 v32, v49, v35
	v_cvt_pk_bf16_f32 v32, v34, v32
	v_lshlrev_b32_e32 v33, 16, v29
	v_and_b32_e32 v34, 0xffff0000, v29
	v_sub_f32_e32 v33, v50, v33
	v_sub_f32_e32 v34, v51, v34
	v_cvt_pk_bf16_f32 v33, v33, v34
	v_cvt_pk_bf16_f32 v34, v52, v53
	v_cvt_pk_bf16_f32 v35, v54, v55
	v_and_b32_e32 v41, 0xffff0000, v36
	v_lshlrev_b32_e32 v38, 16, v34
	v_and_b32_e32 v39, 0xffff0000, v34
	v_sub_f32_e32 v38, v52, v38
	v_sub_f32_e32 v39, v53, v39
	v_cvt_pk_bf16_f32 v38, v38, v39
	v_lshlrev_b32_e32 v39, 16, v35
	v_and_b32_e32 v40, 0xffff0000, v35
	v_sub_f32_e32 v39, v54, v39
	v_sub_f32_e32 v40, v55, v40
	v_cvt_pk_bf16_f32 v39, v39, v40
	v_lshlrev_b32_e32 v40, 16, v36
	v_sub_f32_e32 v40, v56, v40
	v_sub_f32_e32 v41, v57, v41
	v_cvt_pk_bf16_f32 v40, v40, v41
	v_lshlrev_b32_e32 v41, 16, v37
	v_and_b32_e32 v42, 0xffff0000, v37
	v_sub_f32_e32 v41, v58, v41
	v_sub_f32_e32 v42, v59, v42
	v_cvt_pk_bf16_f32 v41, v41, v42
	v_cvt_pk_bf16_f32 v42, v60, v61
	v_and_b32_e32 v48, 0xffff0000, v43
	v_lshlrev_b32_e32 v46, 16, v42
	v_and_b32_e32 v47, 0xffff0000, v42
	v_sub_f32_e32 v46, v60, v46
	v_sub_f32_e32 v47, v61, v47
	v_cvt_pk_bf16_f32 v46, v46, v47
	v_lshlrev_b32_e32 v47, 16, v43
	v_sub_f32_e32 v47, v70, v47
	v_sub_f32_e32 v48, v71, v48
	s_waitcnt vmcnt(11)
	v_cvt_pk_bf16_f32 v44, v72, v73
	v_cvt_pk_bf16_f32 v47, v47, v48
	s_waitcnt vmcnt(9)
	v_cvt_pk_bf16_f32 v45, v74, v75
	s_waitcnt vmcnt(5)
	v_cvt_pk_bf16_f32 v51, v78, v79
	s_waitcnt vmcnt(3)
	v_cvt_pk_bf16_f32 v52, v80, v81
	s_waitcnt vmcnt(1)
	v_cvt_pk_bf16_f32 v53, v82, v83
	v_lshlrev_b32_e32 v48, 16, v44
	v_and_b32_e32 v49, 0xffff0000, v44
	v_sub_f32_e32 v48, v72, v48
	v_sub_f32_e32 v49, v73, v49
	v_cvt_pk_bf16_f32 v48, v48, v49
	v_lshlrev_b32_e32 v49, 16, v45
	v_and_b32_e32 v50, 0xffff0000, v45
	v_sub_f32_e32 v49, v74, v49
	v_sub_f32_e32 v50, v75, v50
	v_cvt_pk_bf16_f32 v49, v49, v50
	v_cvt_pk_bf16_f32 v50, v76, v77
	v_and_b32_e32 v56, 0xffff0000, v51
	v_lshlrev_b32_e32 v54, 16, v50
	v_and_b32_e32 v55, 0xffff0000, v50
	v_sub_f32_e32 v54, v76, v54
	v_sub_f32_e32 v55, v77, v55
	v_cvt_pk_bf16_f32 v54, v54, v55
	v_lshlrev_b32_e32 v55, 16, v51
	v_sub_f32_e32 v55, v78, v55
	v_sub_f32_e32 v56, v79, v56
	v_cvt_pk_bf16_f32 v55, v55, v56
	v_lshlrev_b32_e32 v56, 16, v52
	v_and_b32_e32 v57, 0xffff0000, v52
	v_sub_f32_e32 v56, v80, v56
	v_sub_f32_e32 v57, v81, v57
	v_cvt_pk_bf16_f32 v56, v56, v57
	v_lshlrev_b32_e32 v57, 16, v53
	v_and_b32_e32 v58, 0xffff0000, v53
	v_sub_f32_e32 v57, v82, v57
	v_sub_f32_e32 v58, v83, v58
	v_cvt_pk_bf16_f32 v57, v57, v58
	s_waitcnt vmcnt(0)
	v_cvt_pk_bf16_f32 v58, v84, v62
	v_cvt_pk_bf16_f32 v59, v63, v64
	v_cvt_pk_bf16_f32 v60, v65, v66
	v_cvt_pk_bf16_f32 v61, v68, v69
	s_waitcnt lgkmcnt(0)
	v_lshlrev_b32_e32 v70, 16, v58
	v_and_b32_e32 v71, 0xffff0000, v58
	v_sub_f32_e32 v70, v84, v70
	v_sub_f32_e32 v62, v62, v71
	v_cvt_pk_bf16_f32 v62, v70, v62
	v_lshlrev_b32_e32 v70, 16, v59
	v_sub_f32_e32 v63, v63, v70
	v_and_b32_e32 v70, 0xffff0000, v59
	v_sub_f32_e32 v64, v64, v70
	v_cvt_pk_bf16_f32 v63, v63, v64
	v_lshlrev_b32_e32 v64, 16, v60
	v_sub_f32_e32 v64, v65, v64
	v_and_b32_e32 v65, 0xffff0000, v60
	v_sub_f32_e32 v65, v66, v65
	v_cvt_pk_bf16_f32 v64, v64, v65
	v_lshlrev_b32_e32 v65, 16, v61
	v_sub_f32_e32 v65, v68, v65
	v_and_b32_e32 v66, 0xffff0000, v61
	v_lshlrev_b32_e32 v68, 4, v1
	v_sub_f32_e32 v66, v69, v66
	v_cvt_pk_bf16_f32 v65, v65, v66
	s_barrier
	s_cbranch_scc1 .LBB0_805
	s_add_u32 s6, s8, 0x29100000
	s_addc_u32 s7, s9, 0
	s_add_u32 s14, s8, 0x800000
	s_addc_u32 s15, s9, 0
	s_add_i32 s4, s0, s1
	s_ashr_i32 s5, s4, 31
	s_lshl_b32 s3, s60, 4
	s_lshl_b64 s[16:17], s[4:5], 12
	s_add_u32 s16, s6, s16
	s_addc_u32 s17, s7, s17
	s_add_i32 s5, s4, s10
	s_cmpk_lt_i32 s5, 0x4000
	s_cselect_b32 s4, s5, s4
	s_ashr_i32 s5, s4, 31
	s_lshl_b64 s[4:5], s[4:5], 12
	s_add_u32 s4, s6, s4
	v_lshlrev_b32_e32 v66, 3, v1
	s_addc_u32 s5, s7, s5
	global_load_dwordx2 v[132:133], v66, s[16:17] nt
	global_load_dwordx2 v[128:129], v66, s[16:17] offset:512 nt
	global_load_dwordx2 v[124:125], v66, s[16:17] offset:1024 nt
	global_load_dwordx2 v[120:121], v66, s[16:17] offset:1536 nt
	global_load_dwordx2 v[116:117], v66, s[16:17] offset:2048 nt
	global_load_dwordx2 v[112:113], v66, s[16:17] offset:2560 nt
	global_load_dwordx2 v[108:109], v66, s[16:17] offset:3072 nt
	global_load_dwordx2 v[106:107], v66, s[16:17] offset:3584 nt
	global_load_dwordx2 v[122:123], v66, s[4:5] offset:2048 nt
	global_load_dwordx2 v[118:119], v66, s[4:5] offset:2560 nt
	global_load_dwordx2 v[114:115], v66, s[4:5] offset:3072 nt
	global_load_dwordx2 v[110:111], v66, s[4:5] offset:3584 nt
	global_load_dwordx2 v[138:139], v66, s[4:5] nt
	global_load_dwordx2 v[142:143], v66, s[4:5] offset:512 nt
	global_load_dwordx2 v[130:131], v66, s[4:5] offset:1024 nt
	global_load_dwordx2 v[126:127], v66, s[4:5] offset:1536 nt
	v_mbcnt_lo_u32_b32 v69, -1, 0
	v_mbcnt_hi_u32_b32 v70, -1, v69
	v_and_b32_e32 v69, 64, v70
	v_add_u32_e32 v71, 64, v69
	v_xor_b32_e32 v69, 1, v70
	v_cmp_lt_i32_e32 vcc, v69, v71
	v_xor_b32_e32 v72, 2, v70
	s_lshl_b32 s16, s0, 10
	v_cndmask_b32_e32 v69, v70, v69, vcc
	v_cmp_lt_i32_e32 vcc, v72, v71
	s_add_i32 s26, s16, 0
	s_lshl_b32 s16, s0, 7
	v_cndmask_b32_e32 v72, v70, v72, vcc
	v_lshlrev_b32_e32 v184, 2, v72
	v_xor_b32_e32 v72, 4, v70
	v_cmp_lt_i32_e32 vcc, v72, v71
	s_add_i32 s27, s16, 0
	s_add_i32 s16, 0, 0x20000
	v_cndmask_b32_e32 v72, v70, v72, vcc
	v_lshlrev_b32_e32 v185, 2, v72
	v_xor_b32_e32 v72, 8, v70
	v_cmp_lt_i32_e32 vcc, v72, v71
	s_add_i32 s17, 0, 0x22000
	s_mov_b64 s[4:5], 0x25000000
	v_cndmask_b32_e32 v72, v70, v72, vcc
	v_lshlrev_b32_e32 v186, 2, v72
	v_xor_b32_e32 v72, 16, v70
	v_cmp_lt_i32_e32 vcc, v72, v71
	v_lshlrev_b32_e32 v69, 2, v69
	s_lshl_b32 s25, s0, 5
	v_cndmask_b32_e32 v72, v70, v72, vcc
	v_lshlrev_b32_e32 v187, 2, v72
	v_xor_b32_e32 v72, 32, v70
	v_cmp_lt_i32_e32 vcc, v72, v71
	v_add_u32_e32 v189, s16, v68
	v_add_u32_e32 v190, s17, v68
	v_cndmask_b32_e32 v70, v70, v72, vcc
	v_or_b32_e32 v72, 0x400, v68
	v_add_u32_e32 v191, s16, v72
	v_add_u32_e32 v192, s17, v72
	v_or_b32_e32 v72, 0x800, v68
	v_add_u32_e32 v193, s16, v72
	v_add_u32_e32 v194, s17, v72
	v_or_b32_e32 v72, 0xc00, v68
	v_add_u32_e32 v195, s16, v72
	v_add_u32_e32 v196, s17, v72
	v_or_b32_e32 v72, 0x1000, v68
	v_lshlrev_b32_e32 v188, 2, v70
	v_lshl_add_u64 v[70:71], s[8:9], 0, v[66:67]
	v_add_u32_e32 v197, s16, v72
	v_add_u32_e32 v198, s17, v72
	v_or_b32_e32 v72, 0x1400, v68
	v_lshl_add_u64 v[70:71], v[70:71], 0, s[4:5]
	s_lshl_b32 s4, s0, 1
	v_add_u32_e32 v199, s16, v72
	v_add_u32_e32 v200, s17, v72
	v_or_b32_e32 v72, 0x1800, v68
	s_or_b32 s11, s4, 1
	v_add_u32_e32 v201, s16, v72
	v_add_u32_e32 v202, s17, v72
	v_or_b32_e32 v72, 0x1c00, v68
	s_lshl_b32 s5, s0, 13
	s_lshl_b32 s24, s11, 12
	v_add_u32_e32 v203, s16, v72
	v_add_u32_e32 v204, s17, v72
	v_lshl_add_u64 v[72:73], s[6:7], 0, v[66:67]
	v_mov_b32_e32 v205, 0x358637bd
	s_add_i32 s28, 0, 0x10000
	s_mov_b32 s29, s1
	s_waitcnt vmcnt(15)
	v_mov_b64_e32 v[88:89], v[132:133]
	s_waitcnt vmcnt(14)
	v_mov_b64_e32 v[86:87], v[128:129]
	s_waitcnt vmcnt(13)
	v_mov_b64_e32 v[84:85], v[124:125]
	s_waitcnt vmcnt(12)
	v_mov_b64_e32 v[82:83], v[120:121]
	s_waitcnt vmcnt(11)
	v_mov_b64_e32 v[80:81], v[116:117]
	s_waitcnt vmcnt(10)
	v_mov_b64_e32 v[78:79], v[112:113]
	s_waitcnt vmcnt(9)
	v_mov_b64_e32 v[76:77], v[108:109]
	s_waitcnt vmcnt(8)
	v_mov_b64_e32 v[74:75], v[106:107]
	s_waitcnt vmcnt(4)
	v_mov_b64_e32 v[90:91], v[110:111]
	v_mov_b64_e32 v[92:93], v[114:115]
	v_mov_b64_e32 v[94:95], v[118:119]
	v_mov_b64_e32 v[96:97], v[122:123]
	s_waitcnt vmcnt(0)
	v_mov_b64_e32 v[98:99], v[126:127]
	v_mov_b64_e32 v[100:101], v[130:131]
	v_mov_b64_e32 v[102:103], v[142:143]
	v_mov_b64_e32 v[104:105], v[138:139]
	s_branch .LBB0_801

.LBB0_801:
	s_add_i32 s18, s29, s0
	s_add_i32 s6, s18, s10
	s_add_i32 s29, s29, s3
	s_cmpk_gt_i32 s29, 0x3fff
	s_cselect_b64 s[16:17], -1, 0
	s_and_b64 vcc, exec, s[16:17]
	s_cbranch_vccnz .LBB0_803
	s_add_i32 s20, s6, s10
	s_ashr_i32 s21, s20, 31
	s_lshl_b64 s[22:23], s[20:21], 12
	s_add_i32 s7, s20, s10
	s_cmpk_lt_i32 s7, 0x4000
	s_cselect_b32 s20, s7, s20
	s_ashr_i32 s21, s20, 31
	s_lshl_b64 s[20:21], s[20:21], 12
	v_lshl_add_u64 v[74:75], v[72:73], 0, s[22:23]
	v_lshl_add_u64 v[90:91], v[72:73], 0, s[20:21]
	global_load_dwordx2 v[88:89], v[74:75], off nt
	global_load_dwordx2 v[86:87], v[74:75], off offset:512 nt
	global_load_dwordx2 v[84:85], v[74:75], off offset:1024 nt
	global_load_dwordx2 v[82:83], v[74:75], off offset:1536 nt
	global_load_dwordx2 v[80:81], v[74:75], off offset:2048 nt
	global_load_dwordx2 v[78:79], v[74:75], off offset:2560 nt
	global_load_dwordx2 v[76:77], v[74:75], off offset:3072 nt
	s_nop 0
	global_load_dwordx2 v[74:75], v[74:75], off offset:3584 nt
	s_nop 0
	global_load_dwordx2 v[104:105], v[90:91], off nt
	global_load_dwordx2 v[102:103], v[90:91], off offset:512 nt
	global_load_dwordx2 v[100:101], v[90:91], off offset:1024 nt
	global_load_dwordx2 v[98:99], v[90:91], off offset:1536 nt
	global_load_dwordx2 v[96:97], v[90:91], off offset:2048 nt
	global_load_dwordx2 v[94:95], v[90:91], off offset:2560 nt
	global_load_dwordx2 v[92:93], v[90:91], off offset:3072 nt
	s_nop 0
	global_load_dwordx2 v[90:91], v[90:91], off offset:3584 nt

.LBB0_808:
	v_lshl_add_u64 v[134:135], s[8:9], 0, v[132:133]
	v_add_co_u32_e32 v66, vcc, 0x29100000, v134
	s_nop 1
	v_addc_co_u32_e32 v67, vcc, 0, v135, vcc
	global_load_dwordx2 v[160:161], v[66:67], off offset:1536 nt
	global_load_dwordx2 v[162:163], v[66:67], off offset:2048 nt
	global_load_dwordx2 v[164:165], v[66:67], off offset:3072 nt
	global_load_dwordx2 v[166:167], v[66:67], off offset:3584 nt
	global_load_dwordx2 v[168:169], v[66:67], off offset:512 nt
	global_load_dwordx2 v[170:171], v[66:67], off offset:1024 nt
	global_load_dwordx2 v[172:173], v[66:67], off nt
	global_load_dwordx2 v[174:175], v[66:67], off offset:2560 nt
	global_load_dwordx4 v[74:77], v[92:93], off nt
	s_waitcnt lgkmcnt(0)
	global_load_dwordx4 v[66:69], v[94:95], off nt
	global_load_dwordx4 v[70:73], v[90:91], off nt
	global_load_dwordx4 v[86:89], v[90:91], off offset:1024 nt
	global_load_dwordx4 v[82:85], v[96:97], off nt
	global_load_dwordx4 v[78:81], v[98:99], off nt
	global_load_dwordx4 v[144:147], v[100:101], off nt
	global_load_dwordx4 v[148:151], v[102:103], off nt
	global_load_dwordx4 v[152:155], v[90:91], off offset:2048 nt
	global_load_dwordx4 v[156:159], v[90:91], off offset:3072 nt
	v_add_co_u32_e32 v134, vcc, s11, v134
	s_waitcnt vmcnt(17)
	v_lshlrev_b32_e32 v216, 16, v160
	v_and_b32_e32 v217, 0xffff0000, v160
	s_waitcnt vmcnt(16)
	v_lshlrev_b32_e32 v218, 16, v162
	v_and_b32_e32 v143, 0xffff0000, v162
	s_waitcnt vmcnt(13)
	v_and_b32_e32 v231, 0xffff0000, v168
	v_and_b32_e32 v235, 0xffff0000, v169
	s_waitcnt vmcnt(11)
	v_and_b32_e32 v230, 0xffff0000, v172
	v_and_b32_e32 v234, 0xffff0000, v173
	v_lshlrev_b32_e32 v220, 16, v163
	v_and_b32_e32 v221, 0xffff0000, v163
	v_lshlrev_b32_e32 v229, 16, v168
	v_lshlrev_b32_e32 v228, 16, v172
	v_lshlrev_b32_e32 v233, 16, v169
	v_lshlrev_b32_e32 v232, 16, v173
	v_and_b32_e32 v239, 0xffff0000, v171
	v_and_b32_e32 v238, 0xffff0000, v170
	v_lshlrev_b32_e32 v240, 16, v161
	v_and_b32_e32 v241, 0xffff0000, v161
	v_pk_mul_f32 v[160:161], v[230:231], v[230:231]
	v_pk_mul_f32 v[162:163], v[234:235], v[234:235]
	v_lshlrev_b32_e32 v222, 16, v164
	v_and_b32_e32 v223, 0xffff0000, v164
	v_lshlrev_b32_e32 v237, 16, v171
	v_lshlrev_b32_e32 v236, 16, v170
	v_lshlrev_b32_e32 v246, 16, v165
	v_and_b32_e32 v247, 0xffff0000, v165
	v_pk_mul_f32 v[164:165], v[238:239], v[238:239]
	v_pk_fma_f32 v[160:161], v[228:229], v[228:229], v[160:161]
	v_pk_fma_f32 v[162:163], v[232:233], v[232:233], v[162:163]
	v_lshlrev_b32_e32 v224, 16, v166
	v_and_b32_e32 v252, 0xffff0000, v166
	v_lshlrev_b32_e32 v226, 16, v167
	v_and_b32_e32 v227, 0xffff0000, v167
	v_mul_f32_e32 v219, v216, v216
	v_mul_f32_e32 v167, v217, v217
	v_mul_f32_e32 v168, v240, v240
	v_mov_b32_e32 v166, v218
	v_pk_fma_f32 v[164:165], v[236:237], v[236:237], v[164:165]
	v_pk_add_f32 v[160:161], v[160:161], v[162:163]
	v_pk_fma_f32 v[168:169], v[240:241], v[240:241], v[168:169] op_sel_hi:[1,1,0]
	v_pk_add_f32 v[166:167], v[218:219], v[166:167]
	v_pk_add_f32 v[162:163], v[164:165], v[164:165] op_sel_hi:[0,1]
	v_pk_add_f32 v[160:161], v[160:161], v[160:161] op_sel_hi:[0,1]
	s_waitcnt vmcnt(10)
	v_and_b32_e32 v245, 0xffff0000, v175
	v_and_b32_e32 v244, 0xffff0000, v174
	v_mul_f32_e32 v170, v218, v218
	v_mul_f32_e32 v168, v143, v143
	v_mov_b32_e32 v171, v167
	v_mul_f32_e32 v162, v220, v220
	v_mul_f32_e32 v160, v221, v221
	v_lshlrev_b32_e32 v243, 16, v175
	v_lshlrev_b32_e32 v242, 16, v174
	v_pk_mul_f32 v[172:173], v[244:245], v[244:245]
	v_pk_add_f32 v[164:165], v[170:171], v[168:169]
	v_pk_add_f32 v[160:161], v[162:163], v[160:161]
	v_mul_f32_e32 v225, v222, v222
	v_mul_f32_e32 v175, v223, v223
	v_mul_f32_e32 v176, v246, v246
	v_mov_b32_e32 v174, v224
	v_pk_fma_f32 v[172:173], v[242:243], v[242:243], v[172:173]
	v_pk_add_f32 v[160:161], v[164:165], v[160:161]
	v_pk_fma_f32 v[176:177], v[246:247], v[246:247], v[176:177] op_sel_hi:[1,1,0]
	v_pk_add_f32 v[174:175], v[224:225], v[174:175]
	v_pk_add_f32 v[172:173], v[172:173], v[172:173] op_sel_hi:[0,1]
	v_pk_add_f32 v[168:169], v[160:161], v[160:161] op_sel_hi:[0,1]
	v_mul_f32_e32 v178, v224, v224
	v_mul_f32_e32 v176, v252, v252
	v_mul_f32_e32 v172, v226, v226
	v_mul_f32_e32 v168, v227, v227
	v_mov_b32_e32 v179, v175
	v_pk_add_f32 v[170:171], v[178:179], v[176:177]
	v_pk_add_f32 v[168:169], v[172:173], v[168:169]
	global_load_dwordx4 v[160:163], v[104:105], off nt
	global_load_dwordx4 v[164:167], v[106:107], off nt
	v_pk_add_f32 v[168:169], v[170:171], v[168:169]
	v_mov_b32_e32 v248, v232
	v_add_f32_e32 v180, v168, v169
	ds_bpermute_b32 v181, v136, v180
	global_load_dwordx4 v[168:171], v[108:109], off nt
	global_load_dwordx4 v[172:175], v[110:111], off nt
	global_load_dwordx4 v[176:179], v[112:113], off nt
	v_mov_b32_e32 v249, v234
	v_mov_b32_e32 v250, v228
	s_waitcnt lgkmcnt(0)
	v_add_f32_e32 v184, v180, v181
	ds_bpermute_b32 v185, v137, v184
	global_load_dwordx4 v[180:183], v[114:115], off nt
	v_mov_b32_e32 v251, v230
	v_mov_b32_e32 v234, v233
	s_waitcnt vmcnt(15)
	v_pk_add_f32 v[76:77], v[76:77], 1.0 op_sel_hi:[1,0]
	s_waitcnt lgkmcnt(0)
	v_add_f32_e32 v196, v184, v185
	ds_bpermute_b32 v197, v138, v196
	global_load_dwordx4 v[184:187], v[116:117], off nt
	global_load_dwordx4 v[188:191], v[118:119], off nt
	global_load_dwordx4 v[192:195], v[120:121], off nt
	v_pk_add_f32 v[74:75], v[74:75], 1.0 op_sel_hi:[1,0]
	v_mov_b32_e32 v230, v229
	s_waitcnt lgkmcnt(0)
	v_add_f32_e32 v204, v196, v197
	ds_bpermute_b32 v205, v139, v204
	global_load_dwordx4 v[196:199], v[122:123], off nt
	global_load_dwordx4 v[200:203], v[124:125], off nt
	v_addc_co_u32_e32 v135, vcc, 0, v135, vcc
	s_waitcnt lgkmcnt(0)
	v_add_f32_e32 v219, v204, v205
	global_load_dwordx4 v[204:207], v[126:127], off nt
	global_load_dwordx4 v[208:211], v[128:129], off nt
	global_load_dwordx4 v[212:215], v[130:131], off nt
	ds_bpermute_b32 v225, v140, v219
	s_waitcnt lgkmcnt(0)
	v_add_f32_e32 v219, v219, v225
	ds_bpermute_b32 v225, v141, v219
	s_waitcnt lgkmcnt(0)
	v_add_f32_e32 v219, v219, v225
	v_fmamk_f32 v219, v219, 0x3a000000, v142
	v_rsq_f32_e32 v232, v219
	v_mov_b32_e32 v219, v143
	v_mov_b32_e32 v225, v252
	v_pk_mul_f32 v[248:249], v[248:249], v[232:233] op_sel_hi:[1,0]
	v_pk_mul_f32 v[250:251], v[250:251], v[232:233] op_sel_hi:[1,0]
	v_pk_mul_f32 v[234:235], v[234:235], v[232:233] op_sel_hi:[1,0]
	s_waitcnt vmcnt(21)
	v_pk_mul_f32 v[70:71], v[70:71], v[250:251]
	v_pk_mul_f32 v[72:73], v[72:73], v[248:249]
	v_pk_fma_f32 v[66:67], v[74:75], v[70:71], v[66:67]
	v_pk_fma_f32 v[68:69], v[76:77], v[72:73], v[68:69]
	s_waitcnt vmcnt(20)
	v_pk_mul_f32 v[72:73], v[88:89], v[234:235]
	s_waitcnt vmcnt(19)
	v_pk_add_f32 v[74:75], v[84:85], 1.0 op_sel_hi:[1,0]
	v_pk_mul_f32 v[70:71], v[230:231], v[232:233] op_sel_hi:[1,0]
	s_waitcnt vmcnt(18)
	v_pk_fma_f32 v[72:73], v[74:75], v[72:73], v[80:81]
	v_mov_b32_e32 v74, v237
	v_mov_b32_e32 v75, v239
	v_pk_mul_f32 v[70:71], v[86:87], v[70:71]
	v_pk_add_f32 v[76:77], v[82:83], 1.0 op_sel_hi:[1,0]
	v_pk_mul_f32 v[74:75], v[232:233], v[74:75] op_sel_hi:[0,1]
	v_pk_fma_f32 v[70:71], v[76:77], v[70:71], v[78:79]
	s_waitcnt vmcnt(15)
	v_pk_mul_f32 v[74:75], v[154:155], v[74:75]
	v_pk_add_f32 v[78:79], v[146:147], 1.0 op_sel_hi:[1,0]
	v_mov_b32_e32 v237, v238
	v_pk_fma_f32 v[74:75], v[78:79], v[74:75], v[150:151]
	v_pk_mul_f32 v[78:79], v[240:241], v[232:233] op_sel_hi:[1,0]
	v_pk_mul_f32 v[76:77], v[232:233], v[236:237] op_sel_hi:[0,1]
	s_waitcnt vmcnt(14)
	v_pk_mul_f32 v[78:79], v[158:159], v[78:79]
	v_pk_mul_f32 v[76:77], v[152:153], v[76:77]
	v_pk_add_f32 v[80:81], v[144:145], 1.0 op_sel_hi:[1,0]
	s_waitcnt vmcnt(13)
	v_pk_add_f32 v[82:83], v[162:163], 1.0 op_sel_hi:[1,0]
	s_waitcnt vmcnt(12)
	v_pk_fma_f32 v[78:79], v[82:83], v[78:79], v[166:167]
	v_pk_mul_f32 v[82:83], v[220:221], v[232:233] op_sel_hi:[1,0]
	v_pk_fma_f32 v[76:77], v[80:81], v[76:77], v[148:149]
	v_pk_mul_f32 v[80:81], v[216:217], v[232:233] op_sel_hi:[1,0]
	v_pk_add_f32 v[84:85], v[160:161], 1.0 op_sel_hi:[1,0]
	s_waitcnt vmcnt(11)
	v_pk_mul_f32 v[82:83], v[82:83], v[170:171]
	s_waitcnt vmcnt(10)
	v_pk_add_f32 v[86:87], v[174:175], 1.0 op_sel_hi:[1,0]
	v_pk_mul_f32 v[80:81], v[156:157], v[80:81]
	s_waitcnt vmcnt(9)
	v_pk_fma_f32 v[82:83], v[82:83], v[86:87], v[178:179]
	v_mov_b32_e32 v86, v243
	v_mov_b32_e32 v87, v245
	v_pk_mul_f32 v[86:87], v[232:233], v[86:87] op_sel_hi:[0,1]
	v_pk_fma_f32 v[80:81], v[84:85], v[80:81], v[164:165]
	v_pk_mul_f32 v[84:85], v[218:219], v[232:233] op_sel_hi:[1,0]
	s_waitcnt vmcnt(8)
	v_pk_mul_f32 v[86:87], v[86:87], v[182:183]
	v_pk_mul_f32 v[84:85], v[84:85], v[168:169]
	v_pk_add_f32 v[88:89], v[172:173], 1.0 op_sel_hi:[1,0]
	s_waitcnt vmcnt(7)
	v_pk_add_f32 v[144:145], v[186:187], 1.0 op_sel_hi:[1,0]
	v_mov_b32_e32 v243, v244
	s_waitcnt vmcnt(6)
	v_pk_fma_f32 v[86:87], v[86:87], v[144:145], v[190:191]
	v_pk_mul_f32 v[144:145], v[246:247], v[232:233] op_sel_hi:[1,0]
	v_pk_fma_f32 v[84:85], v[84:85], v[88:89], v[176:177]
	v_pk_mul_f32 v[88:89], v[232:233], v[242:243] op_sel_hi:[0,1]
	s_waitcnt vmcnt(5)
	v_pk_mul_f32 v[144:145], v[144:145], v[194:195]
	s_waitcnt vmcnt(4)
	v_pk_add_f32 v[148:149], v[198:199], 1.0 op_sel_hi:[1,0]
	v_pk_mul_f32 v[88:89], v[88:89], v[180:181]
	v_pk_add_f32 v[146:147], v[184:185], 1.0 op_sel_hi:[1,0]
	s_waitcnt vmcnt(3)
	v_pk_fma_f32 v[144:145], v[144:145], v[148:149], v[202:203]
	v_pk_mul_f32 v[148:149], v[226:227], v[232:233] op_sel_hi:[1,0]
	v_pk_fma_f32 v[88:89], v[88:89], v[146:147], v[188:189]
	v_pk_mul_f32 v[146:147], v[222:223], v[232:233] op_sel_hi:[1,0]
	s_waitcnt vmcnt(2)
	v_pk_mul_f32 v[148:149], v[148:149], v[206:207]
	s_waitcnt vmcnt(1)
	v_pk_add_f32 v[152:153], v[210:211], 1.0 op_sel_hi:[1,0]
	v_pk_mul_f32 v[146:147], v[146:147], v[192:193]
	v_pk_add_f32 v[150:151], v[196:197], 1.0 op_sel_hi:[1,0]
	s_waitcnt vmcnt(0)
	v_pk_fma_f32 v[148:149], v[148:149], v[152:153], v[214:215]
	v_cvt_pk_bf16_f32 v152, v66, v67
	v_pk_fma_f32 v[146:147], v[146:147], v[150:151], v[200:201]
	v_lshlrev_b32_e32 v168, 16, v152
	v_pk_mul_f32 v[150:151], v[224:225], v[232:233] op_sel_hi:[1,0]
	v_sub_f32_e32 v66, v66, v168
	v_and_b32_e32 v168, 0xffff0000, v152
	v_pk_mul_f32 v[150:151], v[150:151], v[204:205]
	v_pk_add_f32 v[154:155], v[208:209], 1.0 op_sel_hi:[1,0]
	v_sub_f32_e32 v67, v67, v168
	v_pk_fma_f32 v[150:151], v[150:151], v[154:155], v[212:213]
	v_cvt_pk_bf16_f32 v153, v68, v69
	global_store_dwordx2 v[134:135], v[152:153], off
	v_cvt_pk_bf16_f32 v154, v70, v71
	v_cvt_pk_bf16_f32 v155, v72, v73
	global_store_dwordx2 v[134:135], v[154:155], off offset:512
	v_cvt_pk_bf16_f32 v156, v76, v77
	v_cvt_pk_bf16_f32 v157, v74, v75
	global_store_dwordx2 v[134:135], v[156:157], off offset:1024
	v_cvt_pk_bf16_f32 v158, v80, v81
	v_cvt_pk_bf16_f32 v159, v78, v79
	global_store_dwordx2 v[134:135], v[158:159], off offset:1536
	v_cvt_pk_bf16_f32 v160, v84, v85
	v_cvt_pk_bf16_f32 v161, v82, v83
	global_store_dwordx2 v[134:135], v[160:161], off offset:2048
	v_cvt_pk_bf16_f32 v162, v88, v89
	v_cvt_pk_bf16_f32 v163, v86, v87
	global_store_dwordx2 v[134:135], v[162:163], off offset:2560
	v_cvt_pk_bf16_f32 v164, v146, v147
	v_cvt_pk_bf16_f32 v165, v144, v145
	global_store_dwordx2 v[134:135], v[164:165], off offset:3072
	v_cvt_pk_bf16_f32 v166, v150, v151
	v_cvt_pk_bf16_f32 v167, v148, v149
	global_store_dwordx2 v[134:135], v[166:167], off offset:3584
	v_mov_b32_e32 v134, v1
	v_cvt_pk_bf16_f32 v66, v66, v67
	v_lshlrev_b32_e32 v67, 16, v153
	s_barrier
	v_sub_f32_e32 v67, v68, v67
	v_lshlrev_b32_e32 v135, 3, v134
	v_and_b32_e32 v68, 0xffff0000, v153
	v_and_b32_e32 v135, 8, v135
	v_sub_f32_e32 v68, v69, v68
	v_lshrrev_b32_e32 v168, 1, v134
	v_or_b32_e32 v143, s4, v135
	v_cvt_pk_bf16_f32 v67, v67, v68
	v_xor_b32_e32 v68, s3, v168
	v_lshl_add_u32 v68, v68, 4, v143
	v_add_u32_e32 v69, 0, v68
	v_add_u32_e32 v68, s21, v68
	ds_write_b64 v69, v[152:153]
	ds_write_b64 v68, v[66:67]
	v_lshlrev_b32_e32 v68, 16, v154
	v_and_b32_e32 v69, 0xffff0000, v154
	v_sub_f32_e32 v68, v70, v68
	v_sub_f32_e32 v69, v71, v69
	v_cvt_pk_bf16_f32 v68, v68, v69
	v_lshlrev_b32_e32 v69, 16, v155
	v_and_b32_e32 v70, 0xffff0000, v155
	v_sub_f32_e32 v69, v72, v69
	v_sub_f32_e32 v70, v73, v70
	v_cvt_pk_bf16_f32 v69, v69, v70
	v_add_u32_e32 v70, 64, v134
	v_lshrrev_b32_e32 v169, 1, v70
	v_xor_b32_e32 v70, s3, v169
	v_lshl_add_u32 v70, v70, 4, v143
	v_add_u32_e32 v71, 0, v70
	v_add_u32_e32 v70, s21, v70
	ds_write_b64 v71, v[154:155]
	ds_write_b64 v70, v[68:69]
	v_lshlrev_b32_e32 v70, 16, v156
	v_and_b32_e32 v71, 0xffff0000, v156
	v_sub_f32_e32 v70, v76, v70
	v_sub_f32_e32 v71, v77, v71
	v_cvt_pk_bf16_f32 v70, v70, v71
	v_lshlrev_b32_e32 v71, 16, v157
	v_and_b32_e32 v72, 0xffff0000, v157
	v_sub_f32_e32 v71, v74, v71
	v_sub_f32_e32 v72, v75, v72
	v_cvt_pk_bf16_f32 v71, v71, v72
	v_add_u32_e32 v72, 0x80, v134
	v_lshrrev_b32_e32 v170, 1, v72
	v_xor_b32_e32 v72, s3, v170
	v_lshl_add_u32 v72, v72, 4, v143
	v_add_u32_e32 v73, 0, v72
	v_add_u32_e32 v72, s21, v72
	ds_write_b64 v73, v[156:157]
	ds_write_b64 v72, v[70:71]
	v_lshlrev_b32_e32 v72, 16, v158
	v_and_b32_e32 v73, 0xffff0000, v158
	v_sub_f32_e32 v72, v80, v72
	v_sub_f32_e32 v73, v81, v73
	v_cvt_pk_bf16_f32 v72, v72, v73
	v_lshlrev_b32_e32 v73, 16, v159
	v_and_b32_e32 v74, 0xffff0000, v159
	v_sub_f32_e32 v73, v78, v73
	v_sub_f32_e32 v74, v79, v74
	v_cvt_pk_bf16_f32 v73, v73, v74
	v_add_u32_e32 v74, 0xc0, v134
	v_lshrrev_b32_e32 v171, 1, v74
	v_xor_b32_e32 v74, s3, v171
	v_lshl_add_u32 v74, v74, 4, v143
	v_add_u32_e32 v75, 0, v74
	v_add_u32_e32 v74, s21, v74
	ds_write_b64 v75, v[158:159]
	ds_write_b64 v74, v[72:73]
	v_lshlrev_b32_e32 v74, 16, v160
	v_and_b32_e32 v75, 0xffff0000, v160
	v_sub_f32_e32 v74, v84, v74
	v_sub_f32_e32 v75, v85, v75
	v_cvt_pk_bf16_f32 v74, v74, v75
	v_lshlrev_b32_e32 v75, 16, v161
	v_and_b32_e32 v76, 0xffff0000, v161
	v_sub_f32_e32 v75, v82, v75
	v_sub_f32_e32 v76, v83, v76
	v_cvt_pk_bf16_f32 v75, v75, v76
	v_add_u32_e32 v76, 0x100, v134
	v_lshrrev_b32_e32 v82, 1, v76
	v_xor_b32_e32 v76, s3, v82
	v_lshl_add_u32 v76, v76, 4, v143
	v_add_u32_e32 v77, 0, v76
	v_add_u32_e32 v76, s21, v76
	ds_write_b64 v77, v[160:161]
	ds_write_b64 v76, v[74:75]
	v_lshlrev_b32_e32 v76, 16, v162
	v_and_b32_e32 v77, 0xffff0000, v162
	v_sub_f32_e32 v76, v88, v76
	v_sub_f32_e32 v77, v89, v77
	v_cvt_pk_bf16_f32 v76, v76, v77
	v_lshlrev_b32_e32 v77, 16, v163
	v_and_b32_e32 v78, 0xffff0000, v163
	v_sub_f32_e32 v77, v86, v77
	v_sub_f32_e32 v78, v87, v78
	v_cvt_pk_bf16_f32 v77, v77, v78
	v_add_u32_e32 v78, 0x140, v134
	v_lshrrev_b32_e32 v83, 1, v78
	v_xor_b32_e32 v78, s3, v83
	v_lshl_add_u32 v78, v78, 4, v143
	v_add_u32_e32 v79, 0, v78
	v_add_u32_e32 v78, s21, v78
	ds_write_b64 v79, v[162:163]
	ds_write_b64 v78, v[76:77]
	v_lshlrev_b32_e32 v78, 16, v164
	v_and_b32_e32 v79, 0xffff0000, v164
	v_sub_f32_e32 v78, v146, v78
	v_sub_f32_e32 v79, v147, v79
	v_cvt_pk_bf16_f32 v78, v78, v79
	v_lshlrev_b32_e32 v79, 16, v165
	v_and_b32_e32 v80, 0xffff0000, v165
	v_sub_f32_e32 v79, v144, v79
	v_sub_f32_e32 v80, v145, v80
	v_cvt_pk_bf16_f32 v79, v79, v80
	v_add_u32_e32 v80, 0x180, v134
	v_lshrrev_b32_e32 v84, 1, v80
	v_xor_b32_e32 v80, s3, v84
	v_lshl_add_u32 v80, v80, 4, v143
	v_add_u32_e32 v81, 0, v80
	v_add_u32_e32 v80, s21, v80
	ds_write_b64 v81, v[164:165]
	ds_write_b64 v80, v[78:79]
	v_lshlrev_b32_e32 v80, 16, v166
	v_and_b32_e32 v81, 0xffff0000, v166
	v_sub_f32_e32 v80, v150, v80
	v_sub_f32_e32 v81, v151, v81
	v_cvt_pk_bf16_f32 v80, v80, v81
	v_lshlrev_b32_e32 v81, 16, v167
	v_and_b32_e32 v85, 0xffff0000, v167
	v_sub_f32_e32 v81, v148, v81
	v_sub_f32_e32 v85, v149, v85
	v_cvt_pk_bf16_f32 v81, v81, v85
	v_add_u32_e32 v85, 0x1c0, v134
	v_lshrrev_b32_e32 v85, 1, v85
	v_xor_b32_e32 v86, s3, v85
	v_lshl_add_u32 v86, v86, 4, v143
	v_add_u32_e32 v87, 0, v86
	v_add_u32_e32 v86, s21, v86
	ds_write_b64 v87, v[166:167]
	ds_write_b64 v86, v[80:81]
	v_or_b32_e32 v86, s16, v135
	v_xor_b32_e32 v87, s5, v168
	v_lshl_add_u32 v87, v87, 4, v86
	v_add_u32_e32 v88, 0, v87
	v_add_u32_e32 v87, s21, v87
	ds_write_b64 v87, v[66:67]
	v_xor_b32_e32 v66, s5, v169
	v_lshl_add_u32 v66, v66, 4, v86
	v_add_u32_e32 v67, 0, v66
	v_add_u32_e32 v66, s21, v66
	ds_write_b64 v88, v[152:153]
	ds_write_b64 v66, v[68:69]
	v_xor_b32_e32 v66, s5, v170
	v_lshl_add_u32 v66, v66, 4, v86
	ds_write_b64 v67, v[154:155]
	v_add_u32_e32 v67, 0, v66
	v_add_u32_e32 v66, s21, v66
	ds_write_b64 v66, v[70:71]
	v_xor_b32_e32 v66, s5, v171
	v_lshl_add_u32 v66, v66, 4, v86
	ds_write_b64 v67, v[156:157]
	v_add_u32_e32 v67, 0, v66
	v_add_u32_e32 v66, s21, v66
	ds_write_b64 v66, v[72:73]
	v_xor_b32_e32 v66, s5, v82
	v_lshl_add_u32 v66, v66, 4, v86
	ds_write_b64 v67, v[158:159]
	v_add_u32_e32 v67, 0, v66
	v_add_u32_e32 v66, s21, v66
	ds_write_b64 v66, v[74:75]
	v_xor_b32_e32 v66, s5, v83
	v_lshl_add_u32 v66, v66, 4, v86
	ds_write_b64 v67, v[160:161]
	v_add_u32_e32 v67, 0, v66
	v_add_u32_e32 v66, s21, v66
	ds_write_b64 v66, v[76:77]
	v_xor_b32_e32 v66, s5, v84
	v_lshl_add_u32 v66, v66, 4, v86
	ds_write_b64 v67, v[162:163]
	v_add_u32_e32 v67, 0, v66
	v_add_u32_e32 v66, s21, v66
	ds_write_b64 v66, v[78:79]
	v_xor_b32_e32 v66, s5, v85
	v_lshl_add_u32 v66, v66, 4, v86
	ds_write_b64 v67, v[164:165]
	v_add_u32_e32 v67, 0, v66
	ds_write_b64 v67, v[166:167]
	v_add_u32_e32 v66, s21, v66
	v_lshrrev_b32_e32 v67, 4, v134
	ds_write_b64 v66, v[80:81]
	v_and_b32_e32 v66, 15, v134
	v_add_u32_e32 v67, s17, v67
	v_lshlrev_b32_e32 v80, 12, v66
	v_bitop3_b32 v68, v67, v134, 15 bitop3:0x78
	v_lshl_add_u32 v72, v68, 4, v80
	v_add_u32_e32 v68, 0, v72
	s_waitcnt lgkmcnt(0)
	s_barrier
	ds_read_b128 v[68:71], v68
	v_add_u32_e32 v72, s21, v72
	ds_read_b128 v[72:75], v72
	s_waitcnt lgkmcnt(1)
	v_mfma_f32_16x16x32_bf16 v[76:79], v[2:5], v[68:71], 0
	v_cmp_gt_u32_e32 vcc, 32, v134
	s_waitcnt lgkmcnt(0)
	v_mfma_f32_16x16x32_bf16 v[72:75], v[2:5], v[72:75], v[76:79]
	v_mfma_f32_16x16x32_bf16 v[68:71], v[6:9], v[68:71], v[72:75]
	s_nop 6
	v_add_u32_e32 v72, 4, v67
	v_bitop3_b32 v72, v72, v134, 15 bitop3:0x78
	v_lshl_add_u32 v76, v72, 4, v80
	v_add_u32_e32 v72, 0, v76
	ds_read_b128 v[72:75], v72
	v_add_u32_e32 v76, s21, v76
	ds_read_b128 v[76:79], v76
	s_waitcnt lgkmcnt(1)
	v_mfma_f32_16x16x32_bf16 v[68:71], v[10:13], v[72:75], v[68:71]
	s_waitcnt lgkmcnt(0)
	v_mfma_f32_16x16x32_bf16 v[68:71], v[10:13], v[76:79], v[68:71]
	v_mfma_f32_16x16x32_bf16 v[68:71], v[14:17], v[72:75], v[68:71]
	v_add_u32_e32 v72, 8, v67
	v_bitop3_b32 v72, v72, v134, 15 bitop3:0x78
	v_lshl_add_u32 v76, v72, 4, v80
	v_add_u32_e32 v72, 0, v76
	ds_read_b128 v[72:75], v72
	v_add_u32_e32 v76, s21, v76
	ds_read_b128 v[76:79], v76
	s_waitcnt lgkmcnt(1)
	v_mfma_f32_16x16x32_bf16 v[68:71], v[18:21], v[72:75], v[68:71]
	s_waitcnt lgkmcnt(0)
	v_mfma_f32_16x16x32_bf16 v[68:71], v[18:21], v[76:79], v[68:71]
	v_mfma_f32_16x16x32_bf16 v[68:71], v[22:25], v[72:75], v[68:71]
	v_add_u32_e32 v72, 12, v67
	v_bitop3_b32 v72, v72, v134, 15 bitop3:0x78
	v_lshl_add_u32 v76, v72, 4, v80
	v_add_u32_e32 v72, 0, v76
	ds_read_b128 v[72:75], v72
	v_add_u32_e32 v76, s21, v76
	ds_read_b128 v[76:79], v76
	s_waitcnt lgkmcnt(1)
	v_mfma_f32_16x16x32_bf16 v[68:71], v[26:29], v[72:75], v[68:71]
	s_waitcnt lgkmcnt(0)
	v_mfma_f32_16x16x32_bf16 v[68:71], v[26:29], v[76:79], v[68:71]
	v_mfma_f32_16x16x32_bf16 v[68:71], v[30:33], v[72:75], v[68:71]
	v_add_u32_e32 v72, 16, v67
	v_bitop3_b32 v72, v72, v134, 15 bitop3:0x78
	v_lshl_add_u32 v76, v72, 4, v80
	v_add_u32_e32 v72, 0, v76
	ds_read_b128 v[72:75], v72
	v_add_u32_e32 v76, s21, v76
	ds_read_b128 v[76:79], v76
	s_waitcnt lgkmcnt(1)
	v_mfma_f32_16x16x32_bf16 v[68:71], v[34:37], v[72:75], v[68:71]
	s_waitcnt lgkmcnt(0)
	v_mfma_f32_16x16x32_bf16 v[68:71], v[34:37], v[76:79], v[68:71]
	v_mfma_f32_16x16x32_bf16 v[68:71], v[38:41], v[72:75], v[68:71]
	v_add_u32_e32 v72, 20, v67
	v_bitop3_b32 v72, v72, v134, 15 bitop3:0x78
	v_lshl_add_u32 v76, v72, 4, v80
	v_add_u32_e32 v72, 0, v76
	ds_read_b128 v[72:75], v72
	v_add_u32_e32 v76, s21, v76
	ds_read_b128 v[76:79], v76
	s_waitcnt lgkmcnt(1)
	v_mfma_f32_16x16x32_bf16 v[68:71], v[42:45], v[72:75], v[68:71]
	s_waitcnt lgkmcnt(0)
	v_mfma_f32_16x16x32_bf16 v[68:71], v[42:45], v[76:79], v[68:71]
	v_mfma_f32_16x16x32_bf16 v[68:71], v[46:49], v[72:75], v[68:71]
	v_add_u32_e32 v72, 24, v67
	v_bitop3_b32 v72, v72, v134, 15 bitop3:0x78
	v_lshl_add_u32 v76, v72, 4, v80
	v_add_u32_e32 v72, 0, v76
	ds_read_b128 v[72:75], v72
	v_add_u32_e32 v76, s21, v76
	ds_read_b128 v[76:79], v76
	s_waitcnt lgkmcnt(1)
	v_mfma_f32_16x16x32_bf16 v[68:71], v[50:53], v[72:75], v[68:71]
	v_add_u32_e32 v67, 28, v67
	v_bitop3_b32 v67, v67, v134, 15 bitop3:0x78
	v_lshl_add_u32 v67, v67, 4, v80
	s_waitcnt lgkmcnt(0)
	v_mfma_f32_16x16x32_bf16 v[68:71], v[50:53], v[76:79], v[68:71]
	v_mfma_f32_16x16x32_bf16 v[68:71], v[54:57], v[72:75], v[68:71]
	v_add_u32_e32 v72, 0, v67
	ds_read_b128 v[72:75], v72
	v_add_u32_e32 v67, s21, v67
	ds_read_b128 v[76:79], v67
	s_waitcnt lgkmcnt(1)
	v_mfma_f32_16x16x32_bf16 v[68:71], v[58:61], v[72:75], v[68:71]
	v_lshlrev_b32_e32 v67, 6, v66
	s_waitcnt lgkmcnt(0)
	s_barrier
	v_mfma_f32_16x16x32_bf16 v[68:71], v[58:61], v[76:79], v[68:71]
	v_mfma_f32_16x16x32_bf16 v[68:71], v[62:65], v[72:75], v[68:71]
	v_and_b32_e32 v72, -16, v134
	v_add3_u32 v67, s18, v67, v72
	v_bfe_u32 v72, v134, 4, 1
	v_cmp_eq_u32_e64 s[6:7], 0, v72
	s_and_b64 s[22:23], vcc, s[6:7]
	s_nop 2
	ds_write_b128 v67, v[68:71]
	v_lshlrev_b32_e32 v69, 7, v134
	v_lshl_add_u32 v67, v72, 6, s19
	v_lshlrev_b32_e32 v68, 2, v66
	v_and_b32_e32 v69, 0xfffff000, v69
	v_add3_u32 v67, v67, v68, v69
	s_waitcnt lgkmcnt(0)
	s_barrier
	ds_read2st64_b32 v[68:69], v67 offset1:4
	ds_read2st64_b32 v[70:71], v67 offset0:8 offset1:12
	s_waitcnt lgkmcnt(1)
	v_add_f32_e32 v67, 0, v68
	v_add_f32_e32 v67, v67, v69
	s_waitcnt lgkmcnt(0)
	v_add_f32_e32 v67, v67, v70
	v_add_f32_e32 v67, v67, v71
	ds_bpermute_b32 v68, v141, v67
	s_waitcnt lgkmcnt(0)
	v_add_f32_e32 v67, v67, v68
	ds_bpermute_b32 v68, v136, v67
	s_waitcnt lgkmcnt(0)
	v_max_f32_e32 v68, v68, v68
	v_max_f32_e32 v68, v67, v68
	ds_bpermute_b32 v69, v137, v68
	s_waitcnt lgkmcnt(0)
	v_max_f32_e32 v69, v69, v69
	v_max_f32_e32 v68, v68, v69
	ds_bpermute_b32 v69, v138, v68
	s_waitcnt lgkmcnt(0)
	v_max_f32_e32 v69, v69, v69
	v_max_f32_e32 v68, v68, v69
	ds_bpermute_b32 v69, v139, v68
	s_waitcnt lgkmcnt(0)
	v_max_f32_e32 v69, v69, v69
	v_max_f32_e32 v68, v68, v69
	v_sub_f32_e32 v67, v67, v68
	v_mul_f32_e32 v67, 0x3fb8aa3b, v67
	v_exp_f32_e32 v67, v67
	ds_bpermute_b32 v68, v136, v67
	s_waitcnt lgkmcnt(0)
	v_add_f32_e32 v68, v67, v68
	ds_bpermute_b32 v69, v137, v68
	s_waitcnt lgkmcnt(0)
	v_add_f32_e32 v68, v68, v69
	ds_bpermute_b32 v69, v138, v68
	s_waitcnt lgkmcnt(0)
	v_add_f32_e32 v68, v68, v69
	ds_bpermute_b32 v69, v139, v68
	s_and_saveexec_b64 s[6:7], s[22:23]
	s_cbranch_execz .LBB0_807
	s_waitcnt lgkmcnt(0)
	v_add_f32_e32 v68, v68, v69
	v_div_scale_f32 v69, s[22:23], v68, v68, v67
	v_rcp_f32_e32 v70, v69
	v_div_scale_f32 v71, vcc, v67, v68, v67
	v_mul_u32_u24_e32 v66, 0x4100, v66
	v_fma_f32 v72, -v69, v70, 1.0
	v_fmac_f32_e32 v70, v72, v70
	v_mul_f32_e32 v72, v71, v70
	v_fma_f32 v73, -v69, v72, v71
	v_fmac_f32_e32 v72, v73, v70
	v_fma_f32 v69, -v69, v72, v71
	v_div_fmas_f32 v69, v69, v70, v72
	s_add_u32 s22, s8, s0
	v_div_fixup_f32 v67, v69, v68, v67
	v_lshlrev_b32_e32 v66, 2, v66
	s_addc_u32 s23, s9, s20
	global_store_dword v66, v67, s[22:23]
	s_branch .LBB0_807

.LBB0_1304:
	v_readlane_b32 s0, v253, 11
	v_readlane_b32 s1, v253, 12
	s_mov_b32 s3, s1
	s_cmp_lt_i32 s0, 15
	s_cselect_b64 s[0:1], -1, 0
	s_cmp_gt_i32 s3, 14
	s_cselect_b64 s[4:5], -1, 0
	s_and_b64 s[0:1], s[0:1], s[4:5]
	s_andn2_b64 vcc, exec, s[0:1]
	s_cbranch_vccnz .LBB0_1342
	v_readlane_b32 s0, v253, 0
	v_readlane_b32 s1, v253, 1
	v_mov_b32_e32 v1, v0
	s_load_dwordx2 s[4:5], s[0:1], 0x30
	s_load_dwordx2 s[12:13], s[0:1], 0x80
	s_load_dwordx2 s[14:15], s[0:1], 0xa0
	s_load_dwordx2 s[16:17], s[0:1], 0xc0
	s_load_dwordx4 s[8:11], s[0:1], 0xb0
	s_load_dwordx2 s[18:19], s[0:1], 0xd0
	s_movk_i32 s0, 0x2000
	v_lshlrev_b32_e32 v2, 2, v1
	v_ashrrev_i32_e32 v3, 31, v2
	v_lshlrev_b64 v[6:7], 2, v[2:3]
	s_waitcnt lgkmcnt(0)
	v_lshl_add_u64 v[2:3], s[4:5], 0, v[6:7]
	v_add_co_u32_e32 v2, vcc, s0, v2
	v_lshl_add_u64 v[26:27], s[18:19], 0, v[6:7]
	s_nop 0
	v_addc_co_u32_e32 v3, vcc, 0, v3, vcc
	s_mov_b32 s0, 0x70a000
	v_add_co_u32_e32 v14, vcc, s0, v26
	s_mov_b32 s0, 0x71a000
	s_nop 0
	v_addc_co_u32_e32 v15, vcc, 0, v27, vcc
	v_add_co_u32_e32 v16, vcc, s0, v26
	s_mov_b32 s0, 0x718000
	s_nop 0
	v_addc_co_u32_e32 v17, vcc, 0, v27, vcc
	v_add_co_u32_e32 v22, vcc, s0, v26
	s_mov_b32 s0, 0x716000
	s_nop 0
	v_addc_co_u32_e32 v23, vcc, 0, v27, vcc
	v_add_co_u32_e32 v24, vcc, s0, v26
	s_mov_b32 s0, 0x726000
	s_nop 0
	v_addc_co_u32_e32 v25, vcc, 0, v27, vcc
	global_load_dwordx4 v[2:5], v[2:3], off nt
	s_nop 0
	global_load_dwordx4 v[6:9], v[14:15], off nt
	global_load_dwordx4 v[10:13], v[16:17], off nt
	s_nop 0
	global_load_dwordx4 v[14:17], v[22:23], off nt
	global_load_dwordx4 v[18:21], v[24:25], off nt
	v_add_co_u32_e32 v22, vcc, s0, v26
	v_ashrrev_i32_e32 v30, 6, v1
	s_nop 0
	v_addc_co_u32_e32 v23, vcc, 0, v27, vcc
	v_add_co_u32_e32 v26, vcc, 0x724000, v26
	global_load_dwordx4 v[22:25], v[22:23], off nt
	s_nop 0
	v_addc_co_u32_e32 v27, vcc, 0, v27, vcc
	global_load_dwordx4 v[26:29], v[26:27], off nt
	v_lshl_add_u32 v31, v1, 4, 0
	s_movk_i32 s0, 0x4100
	v_lshl_add_u32 v32, s2, 3, v30
	s_mov_b32 s21, 0
	v_cmp_gt_i32_e32 vcc, s0, v32
	s_waitcnt vmcnt(5)
	ds_write_b128 v31, v[6:9]
	s_waitcnt vmcnt(4)
	v_pk_add_f32 v[6:7], v[12:13], 1.0 op_sel_hi:[1,0]
	v_pk_add_f32 v[10:11], v[10:11], 1.0 op_sel_hi:[1,0]
	v_pk_mul_f32 v[8:9], v[4:5], v[6:7]
	v_pk_mul_f32 v[6:7], v[2:3], v[10:11]
	s_waitcnt vmcnt(3)
	ds_write_b128 v31, v[14:17] offset:16384
	s_waitcnt vmcnt(2)
	ds_write_b128 v31, v[18:21] offset:24576
	ds_write_b128 v31, v[6:9] offset:8192
	s_waitcnt vmcnt(1)
	v_pk_add_f32 v[10:11], v[24:25], 1.0 op_sel_hi:[1,0]
	v_pk_add_f32 v[12:13], v[22:23], 1.0 op_sel_hi:[1,0]
	v_pk_mul_f32 v[4:5], v[4:5], v[10:11]
	v_pk_mul_f32 v[2:3], v[2:3], v[12:13]
	s_waitcnt vmcnt(0)
	ds_write_b128 v31, v[26:29] offset:40960
	ds_write_b128 v31, v[2:5] offset:32768
	s_waitcnt lgkmcnt(0)
	s_barrier
	s_and_saveexec_b64 s[22:23], vcc
	s_cbranch_execz .LBB0_1318
	s_lshl_b32 s1, s60, 3
	s_add_u32 s4, s18, 0xa00000
	v_ashrrev_i32_e32 v33, 31, v32
	s_addc_u32 s5, s19, 0
	v_lshlrev_b64 v[2:3], 6, v[32:33]
	v_and_b32_e32 v4, 15, v1
	v_lshl_add_u64 v[2:3], s[4:5], 0, v[2:3]
	v_lshlrev_b32_e32 v4, 2, v4
	v_mov_b32_e32 v5, 0
	v_lshl_add_u64 v[2:3], v[2:3], 0, v[4:5]
	global_load_dword v104, v[2:3], off
	v_and_b32_e32 v1, 63, v1
	v_lshl_add_u64 v[2:3], s[4:5], 0, v[4:5]
	v_lshlrev_b32_e32 v4, 3, v1
	v_lshl_add_u64 v[8:9], s[18:19], 0, v[4:5]
	s_mov_b64 s[4:5], 0x29100000
	v_lshl_add_u64 v[4:5], v[8:9], 0, s[4:5]
	s_mov_b64 s[4:5], 0x25000000
	v_lshl_add_u64 v[6:7], v[8:9], 0, s[4:5]
	s_mov_b64 s[4:5], 0x40600000
	v_lshl_add_u64 v[8:9], v[8:9], 0, s[4:5]
	v_lshl_add_u32 v1, v1, 4, 0
	s_mov_b64 s[24:25], 0
	s_movk_i32 s3, 0x40ff
	s_movk_i32 s4, 0x3fff
	v_mov_b32_e32 v100, 0x358637bd
	v_mbcnt_lo_u32_b32 v101, -1, 0
	v_mov_b32_e32 v102, 0x6000
	s_waitcnt vmcnt(0)
	v_mov_b32_e32 v27, v104
	s_branch .LBB0_1309

.LBB0_1309:
	v_ashrrev_i32_e32 v33, 31, v32
	v_lshlrev_b64 v[28:29], 12, v[32:33]
	v_lshl_add_u64 v[30:31], v[4:5], 0, v[28:29]
	global_load_dwordx2 v[70:71], v[30:31], off nt
	global_load_dwordx2 v[68:69], v[30:31], off offset:512 nt
	global_load_dwordx2 v[66:67], v[30:31], off offset:1024 nt
	global_load_dwordx2 v[64:65], v[30:31], off offset:1536 nt
	global_load_dwordx2 v[62:63], v[30:31], off offset:2048 nt
	global_load_dwordx2 v[54:55], v[30:31], off offset:2560 nt
	global_load_dwordx2 v[52:53], v[30:31], off offset:3072 nt
	global_load_dwordx2 v[48:49], v[30:31], off offset:3584 nt
	v_add_u32_e32 v26, s1, v32
	v_cmp_gt_i32_e32 vcc, s0, v26
	v_cmp_lt_i32_e64 s[6:7], s3, v26
	s_and_saveexec_b64 s[26:27], vcc
	s_cbranch_execz .LBB0_1311
	v_ashrrev_i32_e32 v27, 31, v26
	v_lshlrev_b64 v[34:35], 6, v[26:27]
	v_lshl_add_u64 v[34:35], v[2:3], 0, v[34:35]
	global_load_dword v27, v[34:35], off

.LBB0_1314:
	s_ff1_i32_b32 s28, s5
	v_or_b32_e32 v82, s28, v33
	v_lshlrev_b32_e32 v82, 2, v82
	ds_bpermute_b32 v82, v82, v104
	s_mul_i32 s20, s28, 0x900
	s_waitcnt lgkmcnt(0)
	v_ashrrev_i32_e32 v83, 31, v82
	v_lshl_add_u64 v[82:83], s[20:21], 0, v[82:83]
	v_lshlrev_b64 v[82:83], 12, v[82:83]
	v_lshl_add_u64 v[98:99], v[8:9], 0, v[82:83]
	global_load_dwordx2 v[96:97], v[98:99], off nt
	global_load_dwordx2 v[94:95], v[98:99], off offset:512 nt
	global_load_dwordx2 v[92:93], v[98:99], off offset:1024 nt
	global_load_dwordx2 v[90:91], v[98:99], off offset:1536 nt
	global_load_dwordx2 v[88:89], v[98:99], off offset:2048 nt
	global_load_dwordx2 v[86:87], v[98:99], off offset:2560 nt
	global_load_dwordx2 v[84:85], v[98:99], off offset:3072 nt
	global_load_dwordx2 v[82:83], v[98:99], off offset:3584 nt
	s_add_i32 s20, s5, -1
	s_and_b32 s5, s20, s5
	v_sub_co_u32_e64 v99, s[26:27], s5, 1
	s_ff1_i32_b32 s20, s5
	s_and_b64 vcc, s[26:27], exec
	s_cselect_b32 s28, s28, s20
	v_or_b32_e32 v98, s28, v33
	v_lshlrev_b32_e32 v98, 2, v98
	ds_bpermute_b32 v98, v98, v104
	v_readfirstlane_b32 s28, v99
	s_cbranch_vccnz .LBB0_1316
	s_waitcnt lgkmcnt(0)
	v_ashrrev_i32_e32 v99, 31, v98
	s_mulk_i32 s20, 0x900
	v_lshl_add_u64 v[10:11], s[20:21], 0, v[98:99]
	v_lshlrev_b64 v[10:11], 12, v[10:11]
	v_lshl_add_u64 v[98:99], v[8:9], 0, v[10:11]
	global_load_dwordx2 v[24:25], v[98:99], off nt
	global_load_dwordx2 v[22:23], v[98:99], off offset:512 nt
	global_load_dwordx2 v[20:21], v[98:99], off offset:1024 nt
	global_load_dwordx2 v[18:19], v[98:99], off offset:1536 nt
	global_load_dwordx2 v[16:17], v[98:99], off offset:2048 nt
	global_load_dwordx2 v[14:15], v[98:99], off offset:2560 nt
	global_load_dwordx2 v[12:13], v[98:99], off offset:3072 nt
	global_load_dwordx2 v[10:11], v[98:99], off offset:3584 nt

.LBB0_1793:
	v_readlane_b32 s0, v253, 11
	v_readlane_b32 s1, v253, 12
	s_mov_b32 s3, s1
	s_cmp_lt_i32 s0, 20
	s_cselect_b64 s[0:1], -1, 0
	s_cmp_gt_i32 s3, 19
	s_cselect_b64 s[4:5], -1, 0
	s_and_b64 s[0:1], s[0:1], s[4:5]
	s_andn2_b64 vcc, exec, s[0:1]
	s_cbranch_vccnz .LBB0_1803
	v_readlane_b32 s0, v253, 0
	v_readlane_b32 s1, v253, 1
	s_load_dwordx2 s[4:5], s[0:1], 0x38
	s_load_dwordx2 s[6:7], s[0:1], 0xa8
	s_load_dwordx2 s[8:9], s[0:1], 0xd0
	v_mov_b32_e32 v1, v0
	s_mov_b32 s1, 0x720000
	v_lshlrev_b32_e32 v2, 2, v1
	s_waitcnt lgkmcnt(0)
	s_add_u32 s12, s4, 0x2000
	v_ashrrev_i32_e32 v3, 31, v2
	s_addc_u32 s13, s5, 0
	v_lshlrev_b64 v[6:7], 2, v[2:3]
	v_lshl_add_u64 v[2:3], s[12:13], 0, v[6:7]
	v_lshl_add_u64 v[6:7], s[8:9], 0, v[6:7]
	v_add_co_u32_e32 v14, vcc, s1, v6
	s_mov_b32 s1, 0x71e000
	s_nop 0
	v_addc_co_u32_e32 v15, vcc, 0, v7, vcc
	v_add_co_u32_e32 v16, vcc, s1, v6
	global_load_dwordx4 v[2:5], v[2:3], off nt
	s_nop 0
	v_addc_co_u32_e32 v17, vcc, 0, v7, vcc
	global_load_dwordx4 v[6:9], v[14:15], off nt
	global_load_dwordx4 v[10:13], v[16:17], off nt
	v_readfirstlane_b32 s0, v1
	v_lshrrev_b32_e32 v14, 1, v1
	s_ashr_i32 s0, s0, 6
	v_and_b32_e32 v14, 24, v14
	v_lshl_or_b32 v14, s0, 8, v14
	v_ashrrev_i32_e32 v15, 31, v14
	v_lshlrev_b64 v[14:15], 6, v[14:15]
	v_and_b32_e32 v16, 15, v1
	v_lshl_add_u64 v[14:15], s[6:7], 0, v[14:15]
	v_lshlrev_b32_e32 v66, 2, v16
	v_mov_b32_e32 v67, 0
	v_lshl_add_u64 v[16:17], v[14:15], 0, v[66:67]
	s_mov_b32 s1, 0x21000
	s_mov_b64 s[4:5], 0x20000
	v_add_co_u32_e32 v14, vcc, s1, v16
	v_lshl_add_u64 v[18:19], v[16:17], 0, s[4:5]
	s_nop 0
	v_addc_co_u32_e32 v15, vcc, 0, v17, vcc
	global_load_dword v20, v[14:15], off offset:-4096
	global_load_dword v21, v[18:19], off offset:64
	global_load_dword v22, v[18:19], off offset:128
	global_load_dword v23, v[18:19], off offset:192
	global_load_dword v26, v[18:19], off offset:256
	global_load_dword v27, v[18:19], off offset:320
	global_load_dword v28, v[18:19], off offset:384
	global_load_dword v29, v[18:19], off offset:448
	global_load_dword v30, v[18:19], off offset:2048
	global_load_dword v31, v[18:19], off offset:2112
	global_load_dword v32, v[18:19], off offset:2176
	global_load_dword v33, v[18:19], off offset:2240
	global_load_dword v36, v[18:19], off offset:2304
	global_load_dword v37, v[18:19], off offset:2368
	global_load_dword v38, v[18:19], off offset:2432
	s_nop 0
	global_load_dword v18, v[18:19], off offset:2496
	s_mov_b32 s3, 0x22000
	v_add_co_u32_e32 v24, vcc, s3, v16
	v_lshl_add_u32 v19, v1, 4, 0
	s_nop 0
	v_addc_co_u32_e32 v25, vcc, 0, v17, vcc
	global_load_dword v39, v[14:15], off offset:64
	global_load_dword v40, v[14:15], off offset:128
	global_load_dword v41, v[14:15], off offset:192
	global_load_dword v42, v[14:15], off offset:256
	global_load_dword v43, v[14:15], off offset:320
	global_load_dword v44, v[14:15], off offset:384
	global_load_dword v45, v[14:15], off offset:448
	global_load_dword v46, v[14:15], off
	global_load_dword v47, v[24:25], off offset:2176
	global_load_dword v48, v[24:25], off offset:2240
	global_load_dword v49, v[24:25], off offset:2304
	global_load_dword v50, v[24:25], off offset:2368
	global_load_dword v51, v[24:25], off offset:2432
	global_load_dword v52, v[24:25], off offset:2496
	v_add_u32_e32 v34, 0x20000, v19
	v_add_u32_e32 v19, 0x22000, v19
	s_mov_b32 s3, 0x23000
	s_lshl_b32 s10, s60, 3
	s_lshl_b32 s1, s2, 3
	s_cmpk_gt_i32 s2, 0x7ff
	v_and_b32_e32 v1, 63, v1
	s_waitcnt vmcnt(31)
	v_pk_add_f32 v[8:9], v[8:9], 1.0 op_sel_hi:[1,0]
	v_pk_add_f32 v[6:7], v[6:7], 1.0 op_sel_hi:[1,0]
	v_pk_mul_f32 v[4:5], v[4:5], v[8:9]
	v_pk_mul_f32 v[2:3], v[2:3], v[6:7]
	ds_write_b128 v34, v[2:5]
	s_waitcnt vmcnt(28)
	v_cvt_pk_bf16_f32 v2, v20, v21
	s_nop 0
	v_lshlrev_b32_e32 v6, 16, v2
	v_and_b32_e32 v7, 0xffff0000, v2
	v_sub_f32_e32 v6, v20, v6
	v_sub_f32_e32 v7, v21, v7
	s_waitcnt vmcnt(26)
	v_cvt_pk_bf16_f32 v3, v22, v23
	v_cvt_pk_bf16_f32 v6, v6, v7
	ds_write_b128 v19, v[10:13]
	v_lshlrev_b32_e32 v7, 16, v3
	v_and_b32_e32 v8, 0xffff0000, v3
	v_sub_f32_e32 v7, v22, v7
	v_sub_f32_e32 v8, v23, v8
	s_waitcnt vmcnt(24)
	v_cvt_pk_bf16_f32 v4, v26, v27
	v_cvt_pk_bf16_f32 v7, v7, v8
	global_load_dword v53, v[14:15], off offset:2048
	global_load_dword v54, v[14:15], off offset:2112
	global_load_dword v55, v[14:15], off offset:2176
	global_load_dword v56, v[14:15], off offset:2240
	global_load_dword v57, v[14:15], off offset:2304
	global_load_dword v58, v[14:15], off offset:2368
	global_load_dword v59, v[14:15], off offset:2432
	global_load_dword v60, v[14:15], off offset:2496
	v_lshlrev_b32_e32 v8, 16, v4
	v_and_b32_e32 v9, 0xffff0000, v4
	v_sub_f32_e32 v8, v26, v8
	v_sub_f32_e32 v9, v27, v9
	s_waitcnt vmcnt(30)
	v_cvt_pk_bf16_f32 v5, v28, v29
	v_cvt_pk_bf16_f32 v8, v8, v9
	global_load_dword v61, v[24:25], off offset:64
	v_lshlrev_b32_e32 v9, 16, v5
	v_and_b32_e32 v10, 0xffff0000, v5
	v_sub_f32_e32 v9, v28, v9
	v_sub_f32_e32 v10, v29, v10
	v_cvt_pk_bf16_f32 v9, v9, v10
	s_waitcnt vmcnt(29)
	v_cvt_pk_bf16_f32 v10, v30, v31
	v_add_co_u32_e32 v34, vcc, s3, v16
	v_lshlrev_b32_e32 v14, 16, v10
	v_and_b32_e32 v15, 0xffff0000, v10
	v_sub_f32_e32 v14, v30, v14
	v_sub_f32_e32 v15, v31, v15
	s_waitcnt vmcnt(27)
	v_cvt_pk_bf16_f32 v11, v32, v33
	s_waitcnt vmcnt(25)
	v_cvt_pk_bf16_f32 v12, v36, v37
	v_cvt_pk_bf16_f32 v14, v14, v15
	v_addc_co_u32_e32 v35, vcc, 0, v17, vcc
	v_lshlrev_b32_e32 v15, 16, v11
	v_and_b32_e32 v19, 0xffff0000, v11
	v_lshlrev_b32_e32 v16, 16, v12
	v_and_b32_e32 v17, 0xffff0000, v12
	v_sub_f32_e32 v15, v32, v15
	v_sub_f32_e32 v19, v33, v19
	v_sub_f32_e32 v16, v36, v16
	v_sub_f32_e32 v17, v37, v17
	s_waitcnt vmcnt(23)
	v_cvt_pk_bf16_f32 v13, v38, v18
	v_cvt_pk_bf16_f32 v15, v15, v19
	v_cvt_pk_bf16_f32 v16, v16, v17
	global_load_dword v62, v[34:35], off offset:-4096
	global_load_dword v63, v[24:25], off offset:128
	global_load_dword v64, v[24:25], off offset:192
	global_load_dword v65, v[24:25], off offset:256
	global_load_dword v66, v[24:25], off offset:320
	global_load_dword v68, v[24:25], off offset:384
	global_load_dword v69, v[24:25], off offset:448
	v_lshlrev_b32_e32 v17, 16, v13
	v_and_b32_e32 v19, 0xffff0000, v13
	v_sub_f32_e32 v17, v38, v17
	v_sub_f32_e32 v18, v18, v19
	v_cvt_pk_bf16_f32 v17, v17, v18
	s_waitcnt vmcnt(22)
	v_cvt_pk_bf16_f32 v18, v46, v39
	v_cvt_pk_bf16_f32 v19, v40, v41
	v_cvt_pk_bf16_f32 v20, v42, v43
	v_cvt_pk_bf16_f32 v21, v44, v45
	s_waitcnt vmcnt(12)
	v_cvt_pk_bf16_f32 v27, v55, v56
	v_lshlrev_b32_e32 v22, 16, v18
	v_sub_f32_e32 v22, v46, v22
	global_load_dword v46, v[24:25], off offset:2048
	global_load_dword v70, v[24:25], off offset:2112
	global_load_dword v71, v[34:35], off
	global_load_dword v72, v[34:35], off offset:64
	global_load_dword v73, v[34:35], off offset:128
	global_load_dword v74, v[34:35], off offset:192
	global_load_dword v75, v[34:35], off offset:256
	global_load_dword v76, v[34:35], off offset:320
	global_load_dword v77, v[34:35], off offset:384
	global_load_dword v78, v[34:35], off offset:448
	global_load_dword v79, v[34:35], off offset:2048
	global_load_dword v80, v[34:35], off offset:2112
	global_load_dword v81, v[34:35], off offset:2176
	global_load_dword v82, v[34:35], off offset:2240
	global_load_dword v83, v[34:35], off offset:2304
	global_load_dword v84, v[34:35], off offset:2368
	global_load_dword v85, v[34:35], off offset:2432
	global_load_dword v86, v[34:35], off offset:2496
	v_and_b32_e32 v23, 0xffff0000, v18
	v_sub_f32_e32 v23, v39, v23
	v_cvt_pk_bf16_f32 v22, v22, v23
	v_lshlrev_b32_e32 v23, 16, v19
	v_and_b32_e32 v24, 0xffff0000, v19
	v_sub_f32_e32 v23, v40, v23
	v_sub_f32_e32 v24, v41, v24
	v_cvt_pk_bf16_f32 v23, v23, v24
	v_lshlrev_b32_e32 v24, 16, v20
	v_and_b32_e32 v25, 0xffff0000, v20
	v_sub_f32_e32 v24, v42, v24
	v_sub_f32_e32 v25, v43, v25
	v_cvt_pk_bf16_f32 v24, v24, v25
	v_lshlrev_b32_e32 v25, 16, v21
	v_and_b32_e32 v26, 0xffff0000, v21
	v_sub_f32_e32 v25, v44, v25
	v_sub_f32_e32 v26, v45, v26
	v_cvt_pk_bf16_f32 v25, v25, v26
	v_cvt_pk_bf16_f32 v26, v53, v54
	v_and_b32_e32 v32, 0xffff0000, v27
	v_lshlrev_b32_e32 v30, 16, v26
	v_and_b32_e32 v31, 0xffff0000, v26
	v_sub_f32_e32 v30, v53, v30
	v_sub_f32_e32 v31, v54, v31
	v_cvt_pk_bf16_f32 v30, v30, v31
	v_lshlrev_b32_e32 v31, 16, v27
	v_sub_f32_e32 v31, v55, v31
	v_sub_f32_e32 v32, v56, v32
	s_waitcnt vmcnt(28)
	v_cvt_pk_bf16_f32 v28, v57, v58
	v_cvt_pk_bf16_f32 v31, v31, v32
	s_waitcnt vmcnt(26)
	v_cvt_pk_bf16_f32 v29, v59, v60
	s_waitcnt vmcnt(22)
	v_cvt_pk_bf16_f32 v35, v63, v64
	s_waitcnt vmcnt(20)
	v_cvt_pk_bf16_f32 v36, v65, v66
	s_waitcnt vmcnt(18)
	v_cvt_pk_bf16_f32 v37, v68, v69
	v_lshlrev_b32_e32 v32, 16, v28
	v_and_b32_e32 v33, 0xffff0000, v28
	v_sub_f32_e32 v32, v57, v32
	v_sub_f32_e32 v33, v58, v33
	v_cvt_pk_bf16_f32 v32, v32, v33
	v_lshlrev_b32_e32 v33, 16, v29
	v_and_b32_e32 v34, 0xffff0000, v29
	v_sub_f32_e32 v33, v59, v33
	v_sub_f32_e32 v34, v60, v34
	v_cvt_pk_bf16_f32 v33, v33, v34
	v_cvt_pk_bf16_f32 v34, v62, v61
	v_and_b32_e32 v40, 0xffff0000, v35
	v_lshlrev_b32_e32 v38, 16, v34
	v_and_b32_e32 v39, 0xffff0000, v34
	v_sub_f32_e32 v38, v62, v38
	v_sub_f32_e32 v39, v61, v39
	v_cvt_pk_bf16_f32 v38, v38, v39
	v_lshlrev_b32_e32 v39, 16, v35
	v_sub_f32_e32 v39, v63, v39
	v_sub_f32_e32 v40, v64, v40
	v_cvt_pk_bf16_f32 v39, v39, v40
	v_lshlrev_b32_e32 v40, 16, v36
	v_and_b32_e32 v41, 0xffff0000, v36
	v_sub_f32_e32 v40, v65, v40
	v_sub_f32_e32 v41, v66, v41
	v_cvt_pk_bf16_f32 v40, v40, v41
	v_lshlrev_b32_e32 v41, 16, v37
	v_and_b32_e32 v42, 0xffff0000, v37
	v_sub_f32_e32 v41, v68, v41
	v_sub_f32_e32 v42, v69, v42
	v_cvt_pk_bf16_f32 v41, v41, v42
	s_waitcnt vmcnt(16)
	v_cvt_pk_bf16_f32 v42, v46, v70
	s_nop 0
	v_lshlrev_b32_e32 v53, 16, v42
	v_sub_f32_e32 v46, v46, v53
	v_and_b32_e32 v53, 0xffff0000, v42
	v_sub_f32_e32 v53, v70, v53
	v_cvt_pk_bf16_f32 v43, v47, v48
	v_cvt_pk_bf16_f32 v46, v46, v53
	v_cvt_pk_bf16_f32 v44, v49, v50
	v_cvt_pk_bf16_f32 v45, v51, v52
	s_waitcnt vmcnt(4)
	v_cvt_pk_bf16_f32 v59, v81, v82
	s_waitcnt vmcnt(2)
	v_cvt_pk_bf16_f32 v60, v83, v84
	v_lshlrev_b32_e32 v53, 16, v43
	v_sub_f32_e32 v47, v47, v53
	v_and_b32_e32 v53, 0xffff0000, v43
	v_sub_f32_e32 v48, v48, v53
	v_cvt_pk_bf16_f32 v47, v47, v48
	v_lshlrev_b32_e32 v48, 16, v44
	v_sub_f32_e32 v48, v49, v48
	v_and_b32_e32 v49, 0xffff0000, v44
	v_sub_f32_e32 v49, v50, v49
	v_cvt_pk_bf16_f32 v48, v48, v49
	v_lshlrev_b32_e32 v49, 16, v45
	v_and_b32_e32 v50, 0xffff0000, v45
	v_sub_f32_e32 v49, v51, v49
	v_sub_f32_e32 v50, v52, v50
	v_cvt_pk_bf16_f32 v49, v49, v50
	v_cvt_pk_bf16_f32 v50, v71, v72
	v_cvt_pk_bf16_f32 v51, v73, v74
	v_cvt_pk_bf16_f32 v52, v75, v76
	v_cvt_pk_bf16_f32 v53, v77, v78
	v_and_b32_e32 v64, 0xffff0000, v59
	v_lshlrev_b32_e32 v54, 16, v50
	v_and_b32_e32 v55, 0xffff0000, v50
	v_sub_f32_e32 v54, v71, v54
	v_sub_f32_e32 v55, v72, v55
	v_cvt_pk_bf16_f32 v54, v54, v55
	v_lshlrev_b32_e32 v55, 16, v51
	v_and_b32_e32 v56, 0xffff0000, v51
	v_sub_f32_e32 v55, v73, v55
	v_sub_f32_e32 v56, v74, v56
	v_cvt_pk_bf16_f32 v55, v55, v56
	v_lshlrev_b32_e32 v56, 16, v52
	v_and_b32_e32 v57, 0xffff0000, v52
	v_sub_f32_e32 v56, v75, v56
	v_sub_f32_e32 v57, v76, v57
	v_cvt_pk_bf16_f32 v56, v56, v57
	v_lshlrev_b32_e32 v57, 16, v53
	v_and_b32_e32 v58, 0xffff0000, v53
	v_sub_f32_e32 v57, v77, v57
	v_sub_f32_e32 v58, v78, v58
	v_cvt_pk_bf16_f32 v57, v57, v58
	v_cvt_pk_bf16_f32 v58, v79, v80
	v_sub_f32_e32 v64, v82, v64
	v_lshlrev_b32_e32 v62, 16, v58
	v_and_b32_e32 v63, 0xffff0000, v58
	v_sub_f32_e32 v62, v79, v62
	v_sub_f32_e32 v63, v80, v63
	v_cvt_pk_bf16_f32 v62, v62, v63
	v_lshlrev_b32_e32 v63, 16, v59
	v_sub_f32_e32 v63, v81, v63
	v_cvt_pk_bf16_f32 v63, v63, v64
	v_lshlrev_b32_e32 v64, 16, v60
	v_and_b32_e32 v65, 0xffff0000, v60
	v_sub_f32_e32 v64, v83, v64
	v_sub_f32_e32 v65, v84, v65
	s_waitcnt vmcnt(0)
	v_cvt_pk_bf16_f32 v61, v85, v86
	v_cvt_pk_bf16_f32 v64, v64, v65
	s_waitcnt lgkmcnt(0)
	v_lshlrev_b32_e32 v65, 16, v61
	v_sub_f32_e32 v65, v85, v65
	v_and_b32_e32 v66, 0xffff0000, v61
	v_sub_f32_e32 v66, v86, v66
	v_cvt_pk_bf16_f32 v65, v65, v66
	s_barrier
	s_cbranch_scc1 .LBB0_1801
	s_add_u32 s6, s8, 0x29100000
	s_addc_u32 s7, s9, 0
	s_add_u32 s14, s8, 0x800000
	s_addc_u32 s15, s9, 0
	s_add_i32 s4, s0, s1
	s_ashr_i32 s5, s4, 31
	s_lshl_b32 s3, s60, 4
	s_lshl_b64 s[16:17], s[4:5], 12
	s_add_u32 s16, s6, s16
	s_addc_u32 s17, s7, s17
	s_add_i32 s5, s4, s10
	s_cmpk_lt_i32 s5, 0x4000
	s_cselect_b32 s4, s5, s4
	s_ashr_i32 s5, s4, 31
	s_lshl_b64 s[4:5], s[4:5], 12
	s_add_u32 s4, s6, s4
	v_lshlrev_b32_e32 v66, 3, v1
	s_addc_u32 s5, s7, s5
	global_load_dwordx2 v[132:133], v66, s[16:17] nt
	global_load_dwordx2 v[126:127], v66, s[16:17] offset:512 nt
	global_load_dwordx2 v[122:123], v66, s[16:17] offset:1024 nt
	global_load_dwordx2 v[118:119], v66, s[16:17] offset:1536 nt
	global_load_dwordx2 v[114:115], v66, s[16:17] offset:2048 nt
	global_load_dwordx2 v[110:111], v66, s[16:17] offset:2560 nt
	global_load_dwordx2 v[106:107], v66, s[16:17] offset:3072 nt
	global_load_dwordx2 v[104:105], v66, s[16:17] offset:3584 nt
	global_load_dwordx2 v[138:139], v66, s[4:5] nt
	global_load_dwordx2 v[136:137], v66, s[4:5] offset:512 nt
	global_load_dwordx2 v[128:129], v66, s[4:5] offset:1024 nt
	global_load_dwordx2 v[124:125], v66, s[4:5] offset:1536 nt
	global_load_dwordx2 v[120:121], v66, s[4:5] offset:2048 nt
	global_load_dwordx2 v[116:117], v66, s[4:5] offset:2560 nt
	global_load_dwordx2 v[112:113], v66, s[4:5] offset:3072 nt
	global_load_dwordx2 v[108:109], v66, s[4:5] offset:3584 nt
	v_mbcnt_lo_u32_b32 v68, -1, 0
	v_mbcnt_hi_u32_b32 v68, -1, v68
	v_and_b32_e32 v69, 64, v68
	v_add_u32_e32 v69, 64, v69
	v_xor_b32_e32 v70, 1, v68
	v_cmp_lt_i32_e32 vcc, v70, v69
	s_lshl_b32 s16, s0, 10
	s_add_i32 s26, s16, 0
	v_cndmask_b32_e32 v70, v68, v70, vcc
	v_lshlrev_b32_e32 v182, 2, v70
	v_xor_b32_e32 v70, 2, v68
	v_cmp_lt_i32_e32 vcc, v70, v69
	s_lshl_b32 s16, s0, 7
	s_add_i32 s27, s16, 0
	v_cndmask_b32_e32 v70, v68, v70, vcc
	v_lshlrev_b32_e32 v183, 2, v70
	v_xor_b32_e32 v70, 4, v68
	v_cmp_lt_i32_e32 vcc, v70, v69
	s_add_i32 s16, 0, 0x20000
	s_add_i32 s17, 0, 0x22000
	v_cndmask_b32_e32 v70, v68, v70, vcc
	v_lshlrev_b32_e32 v184, 2, v70
	v_xor_b32_e32 v70, 8, v68
	v_cmp_lt_i32_e32 vcc, v70, v69
	s_mov_b64 s[4:5], 0x25000000
	s_lshl_b32 s25, s0, 5
	v_cndmask_b32_e32 v70, v68, v70, vcc
	v_lshlrev_b32_e32 v185, 2, v70
	v_xor_b32_e32 v70, 16, v68
	v_cmp_lt_i32_e32 vcc, v70, v69
	v_mov_b32_e32 v204, 0x358637bd
	s_add_i32 s28, 0, 0x10000
	v_cndmask_b32_e32 v70, v68, v70, vcc
	v_lshlrev_b32_e32 v186, 2, v70
	v_xor_b32_e32 v70, 32, v68
	v_cmp_lt_i32_e32 vcc, v70, v69
	s_mov_b32 s29, s1
	s_waitcnt vmcnt(15)
	v_mov_b64_e32 v[86:87], v[132:133]
	v_cndmask_b32_e32 v68, v68, v70, vcc
	v_lshlrev_b32_e32 v70, 4, v1
	v_or_b32_e32 v71, 0x400, v70
	v_add_u32_e32 v190, s16, v71
	v_add_u32_e32 v191, s17, v71
	v_or_b32_e32 v71, 0x800, v70
	v_add_u32_e32 v192, s16, v71
	v_add_u32_e32 v193, s17, v71
	v_or_b32_e32 v71, 0xc00, v70
	v_lshlrev_b32_e32 v187, 2, v68
	v_lshl_add_u64 v[68:69], s[8:9], 0, v[66:67]
	v_add_u32_e32 v194, s16, v71
	v_add_u32_e32 v195, s17, v71
	v_or_b32_e32 v71, 0x1000, v70
	v_lshl_add_u64 v[68:69], v[68:69], 0, s[4:5]
	s_lshl_b32 s4, s0, 1
	v_add_u32_e32 v196, s16, v71
	v_add_u32_e32 v197, s17, v71
	v_or_b32_e32 v71, 0x1400, v70
	s_or_b32 s11, s4, 1
	v_add_u32_e32 v188, s16, v70
	v_add_u32_e32 v189, s17, v70
	v_add_u32_e32 v198, s16, v71
	v_add_u32_e32 v199, s17, v71
	v_or_b32_e32 v71, 0x1800, v70
	v_or_b32_e32 v70, 0x1c00, v70
	s_lshl_b32 s5, s0, 13
	s_lshl_b32 s24, s11, 12
	v_add_u32_e32 v200, s16, v71
	v_add_u32_e32 v201, s17, v71
	v_add_u32_e32 v202, s16, v70
	v_add_u32_e32 v203, s17, v70
	v_lshl_add_u64 v[70:71], s[6:7], 0, v[66:67]
	s_waitcnt vmcnt(8)
	v_mov_b64_e32 v[72:73], v[104:105]
	v_mov_b64_e32 v[74:75], v[106:107]
	v_mov_b64_e32 v[76:77], v[110:111]
	v_mov_b64_e32 v[78:79], v[114:115]
	v_mov_b64_e32 v[80:81], v[118:119]
	v_mov_b64_e32 v[82:83], v[122:123]
	v_mov_b64_e32 v[84:85], v[126:127]
	s_waitcnt vmcnt(0)
	v_mov_b64_e32 v[88:89], v[108:109]
	v_mov_b64_e32 v[90:91], v[112:113]
	v_mov_b64_e32 v[92:93], v[116:117]
	v_mov_b64_e32 v[94:95], v[120:121]
	v_mov_b64_e32 v[96:97], v[124:125]
	v_mov_b64_e32 v[98:99], v[128:129]
	v_mov_b64_e32 v[100:101], v[136:137]
	v_mov_b64_e32 v[102:103], v[138:139]
	s_branch .LBB0_1797

.LBB0_1797:
	s_add_i32 s18, s29, s0
	s_add_i32 s6, s18, s10
	s_add_i32 s29, s29, s3
	s_cmpk_gt_i32 s29, 0x3fff
	s_cselect_b64 s[16:17], -1, 0
	s_and_b64 vcc, exec, s[16:17]
	s_cbranch_vccnz .LBB0_1799
	s_add_i32 s20, s6, s10
	s_ashr_i32 s21, s20, 31
	s_lshl_b64 s[22:23], s[20:21], 12
	s_add_i32 s7, s20, s10
	s_cmpk_lt_i32 s7, 0x4000
	s_cselect_b32 s20, s7, s20
	s_ashr_i32 s21, s20, 31
	s_lshl_b64 s[20:21], s[20:21], 12
	v_lshl_add_u64 v[72:73], v[70:71], 0, s[22:23]
	v_lshl_add_u64 v[88:89], v[70:71], 0, s[20:21]
	global_load_dwordx2 v[86:87], v[72:73], off nt
	global_load_dwordx2 v[84:85], v[72:73], off offset:512 nt
	global_load_dwordx2 v[82:83], v[72:73], off offset:1024 nt
	global_load_dwordx2 v[80:81], v[72:73], off offset:1536 nt
	global_load_dwordx2 v[78:79], v[72:73], off offset:2048 nt
	global_load_dwordx2 v[76:77], v[72:73], off offset:2560 nt
	global_load_dwordx2 v[74:75], v[72:73], off offset:3072 nt
	s_nop 0
	global_load_dwordx2 v[72:73], v[72:73], off offset:3584 nt
	s_nop 0
	global_load_dwordx2 v[102:103], v[88:89], off nt
	global_load_dwordx2 v[100:101], v[88:89], off offset:512 nt
	global_load_dwordx2 v[98:99], v[88:89], off offset:1024 nt
	global_load_dwordx2 v[96:97], v[88:89], off offset:1536 nt
	global_load_dwordx2 v[94:95], v[88:89], off offset:2048 nt
	global_load_dwordx2 v[92:93], v[88:89], off offset:2560 nt
	global_load_dwordx2 v[90:91], v[88:89], off offset:3072 nt
	s_nop 0
	global_load_dwordx2 v[88:89], v[88:89], off offset:3584 nt

.LBB0_2293:
	v_readlane_b32 s4, v253, 11
	v_readlane_b32 s5, v253, 12
	s_cmp_lt_i32 s4, 25
	s_cselect_b64 s[0:1], -1, 0
	s_cmp_gt_i32 s5, 24
	s_cselect_b64 s[4:5], -1, 0
	s_and_b64 s[0:1], s[0:1], s[4:5]
	s_andn2_b64 vcc, exec, s[0:1]
	s_cbranch_vccnz .LBB0_2308
	v_readlane_b32 s0, v253, 0
	v_readlane_b32 s1, v253, 1
	s_load_dwordx4 s[4:7], s[0:1], 0xc8
	s_movk_i32 s12, 0x4000
	v_lshlrev_b32_e32 v2, 2, v0
	v_ashrrev_i32_e32 v3, 31, v2
	s_waitcnt lgkmcnt(0)
	v_lshl_add_u64 v[2:3], v[2:3], 2, s[6:7]
	v_add_co_u32_e32 v2, vcc, 0x722000, v2
	v_ashrrev_i32_e32 v1, 6, v0
	s_nop 0
	v_addc_co_u32_e32 v3, vcc, 0, v3, vcc
	global_load_dwordx4 v[2:5], v[2:3], off nt
	v_lshl_add_u32 v32, s2, 3, v1
	s_mov_b32 s3, 0
	v_lshl_add_u32 v6, v0, 4, 0
	v_cmp_gt_i32_e32 vcc, s12, v32
	s_waitcnt vmcnt(0)
	ds_write_b128 v6, v[2:5]
	s_waitcnt lgkmcnt(0)
	s_barrier
	s_and_saveexec_b64 s[8:9], vcc
	s_cbranch_execz .LBB0_2307
	s_lshl_b32 s13, s60, 3
	s_add_u32 s0, s6, 0xa00000
	v_ashrrev_i32_e32 v33, 31, v32
	s_addc_u32 s1, s7, 0
	v_lshlrev_b64 v[2:3], 6, v[32:33]
	v_and_b32_e32 v1, 15, v0
	v_lshl_add_u64 v[2:3], s[0:1], 0, v[2:3]
	v_lshlrev_b32_e32 v34, 2, v1
	v_mov_b32_e32 v35, 0
	v_lshl_add_u64 v[2:3], v[2:3], 0, v[34:35]
	global_load_dword v43, v[2:3], off
	v_and_b32_e32 v33, 63, v0
	v_lshl_add_u32 v28, v33, 4, 0
	ds_read_b128 v[0:3], v28
	ds_read_b128 v[4:7], v28 offset:1024
	ds_read_b128 v[8:11], v28 offset:2048
	ds_read_b128 v[12:15], v28 offset:3072
	ds_read_b128 v[16:19], v28 offset:4096
	ds_read_b128 v[20:23], v28 offset:5120
	ds_read_b128 v[24:27], v28 offset:6144
	ds_read_b128 v[28:31], v28 offset:7168
	v_lshl_add_u64 v[36:37], s[0:1], 0, v[34:35]
	v_lshlrev_b32_e32 v34, 3, v33
	v_lshlrev_b32_e32 v42, 2, v33
	v_lshl_add_u64 v[40:41], s[6:7], 0, v[34:35]
	s_mov_b64 s[0:1], 0x29100000
	v_mbcnt_lo_u32_b32 v33, -1, 0
	v_or_b32_e32 v44, 0x400, v42
	v_or_b32_e32 v46, 0x500, v42
	v_or_b32_e32 v48, 0x600, v42
	v_or_b32_e32 v50, 0x700, v42
	v_lshl_add_u64 v[38:39], v[40:41], 0, s[0:1]
	s_mov_b64 s[0:1], 0x40600000
	v_mbcnt_hi_u32_b32 v33, -1, v33
	v_lshl_add_u64 v[40:41], v[40:41], 0, s[0:1]
	s_mov_b64 s[6:7], 0
	s_movk_i32 s14, 0x3fff
	v_lshlrev_b32_e32 v34, 2, v42
	v_lshlrev_b32_e32 v42, 2, v44
	v_lshlrev_b32_e32 v44, 2, v46
	v_lshlrev_b32_e32 v46, 2, v48
	v_lshlrev_b32_e32 v48, 2, v50
	v_and_b32_e32 v134, 64, v33
	s_waitcnt vmcnt(0)
	v_mov_b32_e32 v33, v43
	s_branch .LBB0_2298

.LBB0_2298:
	v_ashrrev_i32_e32 v67, 31, v32
	v_mov_b32_e32 v66, v32
	v_lshlrev_b64 v[68:69], 12, v[66:67]
	v_lshl_add_u64 v[68:69], v[38:39], 0, v[68:69]
	global_load_dwordx2 v[98:99], v[68:69], off nt
	global_load_dwordx2 v[96:97], v[68:69], off offset:512 nt
	global_load_dwordx2 v[92:93], v[68:69], off offset:1024 nt
	global_load_dwordx2 v[90:91], v[68:69], off offset:1536 nt
	global_load_dwordx2 v[86:87], v[68:69], off offset:2048 nt
	global_load_dwordx2 v[84:85], v[68:69], off offset:2560 nt
	global_load_dwordx2 v[80:81], v[68:69], off offset:3072 nt
	global_load_dwordx2 v[78:79], v[68:69], off offset:3584 nt
	v_add_u32_e32 v32, s13, v32
	v_cmp_gt_i32_e32 vcc, s12, v32
	v_cmp_lt_i32_e64 s[0:1], s14, v32
	s_and_saveexec_b64 s[10:11], vcc
	s_cbranch_execz .LBB0_2300
	v_ashrrev_i32_e32 v33, 31, v32
	v_lshlrev_b64 v[68:69], 6, v[32:33]
	v_lshl_add_u64 v[68:69], v[36:37], 0, v[68:69]
	global_load_dword v33, v[68:69], off

.LBB0_2303:
	s_ff1_i32_b32 s16, s10
	v_or_b32_e32 v45, s16, v134
	v_lshlrev_b32_e32 v45, 2, v45
	ds_bpermute_b32 v116, v45, v43
	s_mul_i32 s2, s16, 0x900
	s_waitcnt lgkmcnt(0)
	v_ashrrev_i32_e32 v117, 31, v116
	v_lshl_add_u64 v[116:117], s[2:3], 0, v[116:117]
	v_lshlrev_b64 v[116:117], 12, v[116:117]
	v_lshl_add_u64 v[116:117], v[40:41], 0, v[116:117]
	global_load_dwordx2 v[130:131], v[116:117], off nt
	global_load_dwordx2 v[128:129], v[116:117], off offset:512 nt
	global_load_dwordx2 v[126:127], v[116:117], off offset:1024 nt
	global_load_dwordx2 v[124:125], v[116:117], off offset:1536 nt
	global_load_dwordx2 v[122:123], v[116:117], off offset:2048 nt
	global_load_dwordx2 v[120:121], v[116:117], off offset:2560 nt
	global_load_dwordx2 v[118:119], v[116:117], off offset:3072 nt
	s_nop 0
	global_load_dwordx2 v[116:117], v[116:117], off offset:3584 nt
	s_add_i32 s2, s10, -1
	s_and_b32 s15, s2, s10
	v_sub_co_u32_e64 v45, s[10:11], s15, 1
	s_ff1_i32_b32 s2, s15
	s_and_b64 vcc, s[10:11], exec
	s_cselect_b32 s16, s16, s2
	v_or_b32_e32 v47, s16, v134
	v_lshlrev_b32_e32 v47, 2, v47
	ds_bpermute_b32 v132, v47, v43
	v_readfirstlane_b32 s16, v45
	s_cbranch_vccnz .LBB0_2305
	s_waitcnt lgkmcnt(0)
	v_ashrrev_i32_e32 v133, 31, v132
	s_mulk_i32 s2, 0x900
	v_lshl_add_u64 v[50:51], s[2:3], 0, v[132:133]
	v_lshlrev_b64 v[50:51], 12, v[50:51]
	v_lshl_add_u64 v[50:51], v[40:41], 0, v[50:51]
	global_load_dwordx2 v[64:65], v[50:51], off nt
	global_load_dwordx2 v[62:63], v[50:51], off offset:512 nt
	global_load_dwordx2 v[60:61], v[50:51], off offset:1024 nt
	global_load_dwordx2 v[58:59], v[50:51], off offset:1536 nt
	global_load_dwordx2 v[56:57], v[50:51], off offset:2048 nt
	global_load_dwordx2 v[54:55], v[50:51], off offset:2560 nt
	global_load_dwordx2 v[52:53], v[50:51], off offset:3072 nt
	s_nop 0
	global_load_dwordx2 v[50:51], v[50:51], off offset:3584 nt
